# combined variant plus shorter post-MFMA wait-state padding before the fp8 GEMM epilogues (32 states instead of 64)
# baseline (speedup 1.0000x reference)
.LBB0_352:
	v_mov_b32_e32 v16, v188
	v_mov_b32_e32 v17, v189
	s_lshl_b32 s4, s54, 8
	s_nop 15
	s_nop 15
	s_add_i32 s4, s4, s73
	v_lshlrev_b32_e32 v18, 4, v16
	v_add_u32_e32 v28, s4, v17
	v_add_u32_e32 v19, v18, v17
	v_and_b32_e32 v33, 3, v17
	v_mul_lo_u32 v17, v17, s78
	v_ashrrev_i32_e32 v19, 2, v19
	v_add_u32_e32 v17, s76, v17
	v_add_u32_e32 v32, v17, v18
	v_mul_lo_u32 v17, v19, s78
	v_add_u32_e32 v17, s76, v17
	v_lshlrev_b32_e32 v178, 4, v33
	v_lshlrev_b32_e32 v26, 3, v16
	v_add_u32_e32 v30, s4, v19
	v_add_u32_e32 v25, v17, v178
	v_cmp_gt_i32_e32 vcc, 2, v16
	v_pk_mul_f32 v[18:19], v[146:147], s[34:35] op_sel_hi:[1,0]
	v_pk_mul_f32 v[16:17], v[144:145], s[34:35] op_sel_hi:[1,0]
	v_pk_mul_f32 v[20:21], v[150:151], s[34:35] op_sel_hi:[1,0]
	v_pk_mul_f32 v[22:23], v[148:149], s[34:35] op_sel_hi:[1,0]
	v_cvt_pk_bf16_f32 v16, v16, v17
	v_cvt_pk_bf16_f32 v17, v18, v19
	v_cvt_pk_bf16_f32 v18, v22, v23
	v_cvt_pk_bf16_f32 v19, v20, v21
	ds_write_b128 v32, v[16:19]
	v_pk_mul_f32 v[18:19], v[162:163], s[34:35] op_sel_hi:[1,0]
	v_pk_mul_f32 v[16:17], v[160:161], s[34:35] op_sel_hi:[1,0]
	v_pk_mul_f32 v[22:23], v[166:167], s[34:35] op_sel_hi:[1,0]
	v_pk_mul_f32 v[20:21], v[164:165], s[34:35] op_sel_hi:[1,0]
	v_cvt_pk_bf16_f32 v34, v16, v17
	v_cvt_pk_bf16_f32 v35, v18, v19
	v_cvt_pk_bf16_f32 v36, v20, v21
	v_cvt_pk_bf16_f32 v37, v22, v23
	v_ashrrev_i32_e32 v31, 31, v30
	s_lshl_b32 s4, s52, 8
	ds_write_b128 v32, v[34:37] offset:64
	v_lshlrev_b64 v[34:35], 13, v[30:31]
	s_ashr_i32 s5, s4, 31
	v_lshl_add_u64 v[42:43], s[14:15], 0, v[34:35]
	ds_read_b128 v[34:37], v25
	ds_read_b128 v[38:41], v25 offset:64
	s_cmp_eq_u32 s52, 15
	s_cselect_b64 s[6:7], -1, 0
	v_lshl_add_u64 v[42:43], s[4:5], 1, v[42:43]
	s_and_b64 s[6:7], s[30:31], s[6:7]
	v_lshl_add_u64 v[42:43], v[42:43], 0, s[12:13]
	s_and_b64 s[6:7], s[6:7], vcc
	v_ashrrev_i32_e32 v27, 31, v26
	v_lshl_add_u64 v[42:43], v[42:43], 0, v[178:179]
	v_ashrrev_i32_e32 v29, 31, v28
	s_waitcnt lgkmcnt(0)
	global_store_dwordx4 v[42:43], v[34:37], off
	global_store_dwordx4 v[42:43], v[38:41], off offset:256
	s_and_saveexec_b64 s[28:29], s[6:7]
	s_cbranch_execz .LBB0_354
	v_lshlrev_b64 v[34:35], 6, v[28:29]
	v_lshl_add_u64 v[34:35], s[18:19], 0, v[34:35]
	v_lshl_add_u64 v[34:35], v[26:27], 2, v[34:35]
	global_store_dwordx4 v[34:35], v[16:19], off
	global_store_dwordx4 v[34:35], v[20:23], off offset:16

.LBB0_1114:
	v_mov_b32_e32 v17, v190
	v_mov_b32_e32 v18, v189
	s_nop 15
	s_nop 15
	s_lshl_b32 s4, s44, 8
	v_lshlrev_b32_e32 v18, 4, v18
	v_mul_lo_u32 v20, v17, s67
	v_add_u32_e32 v19, v18, v17
	v_add3_u32 v30, s65, v20, v18
	v_pk_mul_f32 v[22:23], v[130:131], s[30:31] op_sel_hi:[1,0]
	v_pk_mul_f32 v[20:21], v[128:129], s[30:31] op_sel_hi:[1,0]
	v_pk_mul_f32 v[24:25], v[142:143], s[30:31] op_sel_hi:[1,0]
	v_pk_mul_f32 v[26:27], v[140:141], s[30:31] op_sel_hi:[1,0]
	s_add_i32 s4, s4, s63
	v_ashrrev_i32_e32 v19, 2, v19
	v_lshlrev_b32_e32 v17, 4, v17
	v_cvt_pk_bf16_f32 v20, v20, v21
	v_cvt_pk_bf16_f32 v21, v22, v23
	v_cvt_pk_bf16_f32 v22, v26, v27
	v_cvt_pk_bf16_f32 v23, v24, v25
	v_add_u32_e32 v18, s4, v19
	v_mul_lo_u32 v19, v19, s67
	v_and_b32_e32 v178, 48, v17
	ds_write_b128 v30, v[20:23]
	v_pk_mul_f32 v[22:23], v[162:163], s[30:31] op_sel_hi:[1,0]
	v_pk_mul_f32 v[20:21], v[160:161], s[30:31] op_sel_hi:[1,0]
	v_pk_mul_f32 v[24:25], v[166:167], s[30:31] op_sel_hi:[1,0]
	v_pk_mul_f32 v[26:27], v[164:165], s[30:31] op_sel_hi:[1,0]
	s_lshl_b32 s4, s35, 8
	v_add3_u32 v17, s65, v19, v178
	v_cvt_pk_bf16_f32 v20, v20, v21
	v_cvt_pk_bf16_f32 v21, v22, v23
	v_cvt_pk_bf16_f32 v22, v26, v27
	v_cvt_pk_bf16_f32 v23, v24, v25
	v_ashrrev_i32_e32 v19, 31, v18
	s_ashr_i32 s5, s4, 31
	ds_write_b128 v30, v[20:23] offset:64
	v_lshlrev_b64 v[20:21], 12, v[18:19]
	v_lshl_add_u64 v[20:21], s[18:19], 0, v[20:21]
	s_lshl_b64 s[4:5], s[4:5], 1
	v_lshl_add_u64 v[28:29], v[20:21], 0, s[4:5]
	ds_read_b128 v[20:23], v17
	ds_read_b128 v[24:27], v17 offset:64
	s_mov_b32 s35, s8
	v_lshl_add_u64 v[28:29], v[28:29], 0, s[34:35]
	v_lshl_add_u64 v[28:29], v[28:29], 0, v[178:179]
	s_waitcnt lgkmcnt(0)
	global_store_dwordx4 v[28:29], v[20:23], off
	global_store_dwordx4 v[28:29], v[24:27], off offset:256
	s_nop 0
	v_pk_mul_f32 v[22:23], v[122:123], s[30:31] op_sel_hi:[1,0]
	v_pk_mul_f32 v[20:21], v[120:121], s[30:31] op_sel_hi:[1,0]
	v_pk_mul_f32 v[24:25], v[126:127], s[30:31] op_sel_hi:[1,0]
	v_pk_mul_f32 v[26:27], v[124:125], s[30:31] op_sel_hi:[1,0]
	v_cvt_pk_bf16_f32 v20, v20, v21
	v_cvt_pk_bf16_f32 v21, v22, v23
	v_cvt_pk_bf16_f32 v22, v26, v27
	v_cvt_pk_bf16_f32 v23, v24, v25
	ds_write_b128 v30, v[20:23]
	v_pk_mul_f32 v[22:23], v[146:147], s[30:31] op_sel_hi:[1,0]
	v_pk_mul_f32 v[20:21], v[144:145], s[30:31] op_sel_hi:[1,0]
	v_pk_mul_f32 v[24:25], v[150:151], s[30:31] op_sel_hi:[1,0]
	v_pk_mul_f32 v[26:27], v[148:149], s[30:31] op_sel_hi:[1,0]
	v_cvt_pk_bf16_f32 v20, v20, v21
	v_cvt_pk_bf16_f32 v21, v22, v23
	v_cvt_pk_bf16_f32 v22, v26, v27
	v_cvt_pk_bf16_f32 v23, v24, v25
	ds_write_b128 v30, v[20:23] offset:64
	v_add_u32_e32 v20, 16, v18
	v_ashrrev_i32_e32 v21, 31, v20
	v_lshlrev_b64 v[20:21], 12, v[20:21]
	v_lshl_add_u64 v[28:29], s[18:19], 0, v[20:21]
	ds_read_b128 v[20:23], v17
	ds_read_b128 v[24:27], v17 offset:64
	v_lshl_add_u64 v[28:29], v[28:29], 0, s[4:5]
	v_lshl_add_u64 v[28:29], v[28:29], 0, s[34:35]
	v_lshl_add_u64 v[28:29], v[28:29], 0, v[178:179]
	s_waitcnt lgkmcnt(0)
	global_store_dwordx4 v[28:29], v[20:23], off
	global_store_dwordx4 v[28:29], v[24:27], off offset:256
	s_nop 0
	v_pk_mul_f32 v[22:23], v[98:99], s[30:31] op_sel_hi:[1,0]
	v_pk_mul_f32 v[20:21], v[96:97], s[30:31] op_sel_hi:[1,0]
	v_pk_mul_f32 v[24:25], v[102:103], s[30:31] op_sel_hi:[1,0]
	v_pk_mul_f32 v[26:27], v[100:101], s[30:31] op_sel_hi:[1,0]
	v_cvt_pk_bf16_f32 v20, v20, v21
	v_cvt_pk_bf16_f32 v21, v22, v23
	v_cvt_pk_bf16_f32 v22, v26, v27
	v_cvt_pk_bf16_f32 v23, v24, v25
	ds_write_b128 v30, v[20:23]
	v_pk_mul_f32 v[22:23], v[134:135], s[30:31] op_sel_hi:[1,0]
	v_pk_mul_f32 v[20:21], v[132:133], s[30:31] op_sel_hi:[1,0]
	v_pk_mul_f32 v[24:25], v[138:139], s[30:31] op_sel_hi:[1,0]
	v_pk_mul_f32 v[26:27], v[136:137], s[30:31] op_sel_hi:[1,0]
	v_cvt_pk_bf16_f32 v20, v20, v21
	v_cvt_pk_bf16_f32 v21, v22, v23
	v_cvt_pk_bf16_f32 v22, v26, v27
	v_cvt_pk_bf16_f32 v23, v24, v25
	ds_write_b128 v30, v[20:23] offset:64
	v_add_u32_e32 v20, 32, v18
	v_ashrrev_i32_e32 v21, 31, v20
	v_lshlrev_b64 v[20:21], 12, v[20:21]
	v_lshl_add_u64 v[28:29], s[18:19], 0, v[20:21]
	ds_read_b128 v[20:23], v17
	ds_read_b128 v[24:27], v17 offset:64
	v_lshl_add_u64 v[28:29], v[28:29], 0, s[4:5]
	v_lshl_add_u64 v[28:29], v[28:29], 0, s[34:35]
	v_lshl_add_u64 v[28:29], v[28:29], 0, v[178:179]
	s_waitcnt lgkmcnt(0)
	global_store_dwordx4 v[28:29], v[20:23], off
	global_store_dwordx4 v[28:29], v[24:27], off offset:256
	s_nop 0
	v_pk_mul_f32 v[22:23], v[82:83], s[30:31] op_sel_hi:[1,0]
	v_pk_mul_f32 v[20:21], v[80:81], s[30:31] op_sel_hi:[1,0]
	v_pk_mul_f32 v[24:25], v[86:87], s[30:31] op_sel_hi:[1,0]
	v_pk_mul_f32 v[26:27], v[84:85], s[30:31] op_sel_hi:[1,0]
	v_cvt_pk_bf16_f32 v20, v20, v21
	v_cvt_pk_bf16_f32 v21, v22, v23
	v_cvt_pk_bf16_f32 v22, v26, v27
	v_cvt_pk_bf16_f32 v23, v24, v25
	ds_write_b128 v30, v[20:23]
	v_pk_mul_f32 v[22:23], v[106:107], s[30:31] op_sel_hi:[1,0]
	v_pk_mul_f32 v[20:21], v[104:105], s[30:31] op_sel_hi:[1,0]
	v_pk_mul_f32 v[24:25], v[110:111], s[30:31] op_sel_hi:[1,0]
	v_pk_mul_f32 v[26:27], v[108:109], s[30:31] op_sel_hi:[1,0]
	v_cvt_pk_bf16_f32 v20, v20, v21
	v_cvt_pk_bf16_f32 v21, v22, v23
	v_cvt_pk_bf16_f32 v22, v26, v27
	v_cvt_pk_bf16_f32 v23, v24, v25
	ds_write_b128 v30, v[20:23] offset:64
	v_add_u32_e32 v20, 48, v18
	v_ashrrev_i32_e32 v21, 31, v20
	v_lshlrev_b64 v[20:21], 12, v[20:21]
	v_lshl_add_u64 v[28:29], s[18:19], 0, v[20:21]
	ds_read_b128 v[20:23], v17
	ds_read_b128 v[24:27], v17 offset:64
	v_lshl_add_u64 v[28:29], v[28:29], 0, s[4:5]
	v_lshl_add_u64 v[28:29], v[28:29], 0, s[34:35]
	v_lshl_add_u64 v[28:29], v[28:29], 0, v[178:179]
	s_waitcnt lgkmcnt(0)
	global_store_dwordx4 v[28:29], v[20:23], off
	global_store_dwordx4 v[28:29], v[24:27], off offset:256
	s_nop 0
	v_pk_mul_f32 v[22:23], v[114:115], s[30:31] op_sel_hi:[1,0]
	v_pk_mul_f32 v[20:21], v[112:113], s[30:31] op_sel_hi:[1,0]
	v_pk_mul_f32 v[26:27], v[118:119], s[30:31] op_sel_hi:[1,0]
	v_pk_mul_f32 v[28:29], v[116:117], s[30:31] op_sel_hi:[1,0]
	v_cvt_pk_bf16_f32 v20, v20, v21
	v_cvt_pk_bf16_f32 v21, v22, v23
	v_cvt_pk_bf16_f32 v22, v28, v29
	v_cvt_pk_bf16_f32 v23, v26, v27
	v_add_u32_e32 v24, 0x80, v18
	ds_write_b128 v30, v[20:23]
	v_pk_mul_f32 v[22:23], v[154:155], s[30:31] op_sel_hi:[1,0]
	v_pk_mul_f32 v[20:21], v[152:153], s[30:31] op_sel_hi:[1,0]
	v_pk_mul_f32 v[26:27], v[158:159], s[30:31] op_sel_hi:[1,0]
	v_pk_mul_f32 v[28:29], v[156:157], s[30:31] op_sel_hi:[1,0]
	v_cvt_pk_bf16_f32 v20, v20, v21
	v_cvt_pk_bf16_f32 v21, v22, v23
	v_cvt_pk_bf16_f32 v22, v28, v29
	v_cvt_pk_bf16_f32 v23, v26, v27
	v_ashrrev_i32_e32 v25, 31, v24
	ds_write_b128 v30, v[20:23] offset:64
	v_lshlrev_b64 v[20:21], 12, v[24:25]
	v_lshl_add_u64 v[28:29], s[18:19], 0, v[20:21]
	ds_read_b128 v[20:23], v17
	ds_read_b128 v[24:27], v17 offset:64
	v_lshl_add_u64 v[28:29], v[28:29], 0, s[4:5]
	v_lshl_add_u64 v[28:29], v[28:29], 0, s[34:35]
	v_lshl_add_u64 v[28:29], v[28:29], 0, v[178:179]
	s_waitcnt lgkmcnt(0)
	global_store_dwordx4 v[28:29], v[20:23], off
	global_store_dwordx4 v[28:29], v[24:27], off offset:256
	s_nop 0
	v_pk_mul_f32 v[22:23], v[90:91], s[30:31] op_sel_hi:[1,0]
	v_pk_mul_f32 v[20:21], v[88:89], s[30:31] op_sel_hi:[1,0]
	v_pk_mul_f32 v[24:25], v[94:95], s[30:31] op_sel_hi:[1,0]
	v_pk_mul_f32 v[26:27], v[92:93], s[30:31] op_sel_hi:[1,0]
	v_cvt_pk_bf16_f32 v20, v20, v21
	v_cvt_pk_bf16_f32 v21, v22, v23
	v_cvt_pk_bf16_f32 v22, v26, v27
	v_cvt_pk_bf16_f32 v23, v24, v25
	ds_write_b128 v30, v[20:23]
	v_pk_mul_f32 v[22:23], v[58:59], s[30:31] op_sel_hi:[1,0]
	v_pk_mul_f32 v[20:21], v[56:57], s[30:31] op_sel_hi:[1,0]
	v_pk_mul_f32 v[24:25], v[62:63], s[30:31] op_sel_hi:[1,0]
	v_pk_mul_f32 v[26:27], v[60:61], s[30:31] op_sel_hi:[1,0]
	v_cvt_pk_bf16_f32 v20, v20, v21
	v_cvt_pk_bf16_f32 v21, v22, v23
	v_cvt_pk_bf16_f32 v22, v26, v27
	v_cvt_pk_bf16_f32 v23, v24, v25
	ds_write_b128 v30, v[20:23] offset:64
	v_add_u32_e32 v20, 0x90, v18
	v_ashrrev_i32_e32 v21, 31, v20
	v_lshlrev_b64 v[20:21], 12, v[20:21]
	v_lshl_add_u64 v[28:29], s[18:19], 0, v[20:21]
	ds_read_b128 v[20:23], v17
	ds_read_b128 v[24:27], v17 offset:64
	v_lshl_add_u64 v[28:29], v[28:29], 0, s[4:5]
	v_lshl_add_u64 v[28:29], v[28:29], 0, s[34:35]
	v_pk_mul_f32 v[10:11], v[10:11], s[30:31] op_sel_hi:[1,0]
	v_pk_mul_f32 v[8:9], v[8:9], s[30:31] op_sel_hi:[1,0]
	v_pk_mul_f32 v[14:15], v[14:15], s[30:31] op_sel_hi:[1,0]
	v_pk_mul_f32 v[12:13], v[12:13], s[30:31] op_sel_hi:[1,0]
	v_lshl_add_u64 v[28:29], v[28:29], 0, v[178:179]
	v_cvt_pk_bf16_f32 v8, v8, v9
	v_cvt_pk_bf16_f32 v9, v10, v11
	v_cvt_pk_bf16_f32 v10, v12, v13
	v_cvt_pk_bf16_f32 v11, v14, v15
	s_waitcnt lgkmcnt(0)
	global_store_dwordx4 v[28:29], v[20:23], off
	global_store_dwordx4 v[28:29], v[24:27], off offset:256
	ds_write_b128 v30, v[8:11] offset:64
	v_pk_mul_f32 v[22:23], v[74:75], s[30:31] op_sel_hi:[1,0]
	v_pk_mul_f32 v[20:21], v[72:73], s[30:31] op_sel_hi:[1,0]
	v_pk_mul_f32 v[24:25], v[78:79], s[30:31] op_sel_hi:[1,0]
	v_pk_mul_f32 v[26:27], v[76:77], s[30:31] op_sel_hi:[1,0]
	v_add_u32_e32 v8, 0xa0, v18
	v_cvt_pk_bf16_f32 v20, v20, v21
	v_cvt_pk_bf16_f32 v21, v22, v23
	v_cvt_pk_bf16_f32 v22, v26, v27
	v_cvt_pk_bf16_f32 v23, v24, v25
	v_ashrrev_i32_e32 v9, 31, v8
	ds_write_b128 v30, v[20:23]
	v_lshlrev_b64 v[8:9], 12, v[8:9]
	v_lshl_add_u64 v[20:21], s[18:19], 0, v[8:9]
	ds_read_b128 v[8:11], v17
	ds_read_b128 v[12:15], v17 offset:64
	v_lshl_add_u64 v[20:21], v[20:21], 0, s[4:5]
	v_lshl_add_u64 v[20:21], v[20:21], 0, s[34:35]
	v_lshl_add_u64 v[20:21], v[20:21], 0, v[178:179]
	s_waitcnt lgkmcnt(0)
	global_store_dwordx4 v[20:21], v[8:11], off
	global_store_dwordx4 v[20:21], v[12:15], off offset:256
	s_nop 0
	v_pk_mul_f32 v[10:11], v[70:71], s[30:31] op_sel_hi:[1,0]
	v_pk_mul_f32 v[8:9], v[68:69], s[30:31] op_sel_hi:[1,0]
	v_pk_mul_f32 v[12:13], v[66:67], s[30:31] op_sel_hi:[1,0]
	v_pk_mul_f32 v[14:15], v[64:65], s[30:31] op_sel_hi:[1,0]
	v_cvt_pk_bf16_f32 v8, v8, v9
	v_cvt_pk_bf16_f32 v9, v10, v11
	v_cvt_pk_bf16_f32 v10, v14, v15
	v_cvt_pk_bf16_f32 v11, v12, v13
	ds_write_b128 v30, v[8:11]
	v_pk_mul_f32 v[6:7], v[6:7], s[30:31] op_sel_hi:[1,0]
	v_pk_mul_f32 v[4:5], v[4:5], s[30:31] op_sel_hi:[1,0]
	v_pk_mul_f32 v[8:9], v[2:3], s[30:31] op_sel_hi:[1,0]
	v_pk_mul_f32 v[2:3], v[0:1], s[30:31] op_sel_hi:[1,0]
	v_cvt_pk_bf16_f32 v0, v4, v5
	v_cvt_pk_bf16_f32 v1, v6, v7
	v_cvt_pk_bf16_f32 v2, v2, v3
	v_cvt_pk_bf16_f32 v3, v8, v9
	ds_write_b128 v30, v[0:3] offset:64
	v_add_u32_e32 v0, 0xb0, v18
	v_ashrrev_i32_e32 v1, 31, v0
	v_lshlrev_b64 v[0:1], 12, v[0:1]
	v_lshl_add_u64 v[8:9], s[18:19], 0, v[0:1]
	ds_read_b128 v[0:3], v17
	ds_read_b128 v[4:7], v17 offset:64
	v_lshl_add_u64 v[8:9], v[8:9], 0, s[4:5]
	v_lshl_add_u64 v[8:9], v[8:9], 0, s[34:35]
	v_lshl_add_u64 v[8:9], v[8:9], 0, v[178:179]
	s_mov_b64 s[4:5], -1
	s_andn2_b64 vcc, exec, s[2:3]
	s_mov_b32 s35, s36
	s_mov_b32 s44, s38
	s_mov_b64 s[46:47], s[42:43]
	s_mov_b64 s[48:49], s[40:41]
	s_waitcnt lgkmcnt(0)
	global_store_dwordx4 v[8:9], v[0:3], off
	global_store_dwordx4 v[8:9], v[4:7], off offset:256
	s_cbranch_vccz .LBB0_1133

.LBB0_1370:
	v_mov_b32_e32 v1, v200
	v_mov_b32_e32 v3, v201
	s_nop 15
	s_nop 15
	s_lshl_b32 s4, s75, 8
	v_lshl_add_u32 v2, v1, 4, v3
	v_ashrrev_i32_e32 v2, 1, v2
	v_lshlrev_b32_e32 v4, 4, v3
	v_and_b32_e32 v170, 16, v4
	v_and_b32_e32 v4, -16, v2
	s_add_i32 s4, s4, s60
	v_add_u32_e32 v4, s4, v4
	v_lshlrev_b32_e32 v12, 3, v1
	v_mul_lo_u32 v1, v2, 48
	v_and_or_b32 v2, v2, 15, v4
	v_pk_mul_f32 v[4:5], v[196:197], s[42:43] op_sel_hi:[1,0]
	v_mul_lo_u32 v3, v3, 48
	v_mul_f32_e32 v6, 0xbfb8aa3b, v5
	v_exp_f32_e32 v8, v6
	v_pk_mul_f32 v[6:7], v[124:125], s[42:43] op_sel_hi:[1,0]
	v_pk_mul_f32 v[42:43], v[42:43], s[42:43] op_sel_hi:[1,0]
	v_mul_f32_e32 v9, 0xbfb8aa3b, v7
	v_exp_f32_e32 v9, v9
	v_add_f32_e32 v8, 1.0, v8
	v_rcp_f32_e32 v8, v8
	v_add3_u32 v1, s63, v1, v170
	v_add_f32_e32 v9, 1.0, v9
	v_rcp_f32_e32 v9, v9
	v_mul_f32_e32 v5, v5, v8
	v_mul_f32_e32 v10, v4, v5
	v_pk_mul_f32 v[4:5], v[194:195], s[42:43] op_sel_hi:[1,0]
	v_mul_f32_e32 v7, v7, v9
	v_mul_f32_e32 v8, 0xbfb8aa3b, v5
	v_exp_f32_e32 v11, v8
	v_pk_mul_f32 v[8:9], v[126:127], s[42:43] op_sel_hi:[1,0]
	v_mul_f32_e32 v14, v6, v7
	v_mul_f32_e32 v13, 0xbfb8aa3b, v9
	v_exp_f32_e32 v13, v13
	v_add_f32_e32 v6, 1.0, v11
	v_rcp_f32_e32 v11, v6
	s_lshl_b32 s4, s48, 7
	v_add_f32_e32 v6, 1.0, v13
	v_rcp_f32_e32 v13, v6
	v_pk_mul_f32 v[6:7], v[192:193], s[42:43] op_sel_hi:[1,0]
	v_mul_f32_e32 v5, v5, v11
	v_mul_f32_e32 v15, 0xbfb8aa3b, v7
	v_exp_f32_e32 v15, v15
	v_mul_f32_e32 v11, v4, v5
	v_mul_f32_e32 v9, v9, v13
	v_mul_f32_e32 v56, v8, v9
	v_add_f32_e32 v4, 1.0, v15
	v_rcp_f32_e32 v13, v4
	v_pk_mul_f32 v[4:5], v[120:121], s[42:43] op_sel_hi:[1,0]
	s_ashr_i32 s5, s4, 31
	v_mul_f32_e32 v15, 0xbfb8aa3b, v5
	v_exp_f32_e32 v15, v15
	v_mul_f32_e32 v7, v7, v13
	v_mul_f32_e32 v13, v6, v7
	v_pk_mul_f32 v[32:33], v[32:33], s[42:43] op_sel_hi:[1,0]
	v_add_f32_e32 v6, 1.0, v15
	v_rcp_f32_e32 v15, v6
	v_pk_mul_f32 v[6:7], v[190:191], s[42:43] op_sel_hi:[1,0]
	v_pk_mul_f32 v[16:17], v[16:17], s[42:43] op_sel_hi:[1,0]
	v_mul_f32_e32 v8, 0xbfb8aa3b, v7
	v_exp_f32_e32 v57, v8
	v_pk_mul_f32 v[8:9], v[122:123], s[42:43] op_sel_hi:[1,0]
	v_mul_f32_e32 v5, v5, v15
	v_mul_f32_e32 v58, 0xbfb8aa3b, v9
	v_exp_f32_e32 v58, v58
	v_add_f32_e32 v15, 1.0, v57
	v_rcp_f32_e32 v15, v15
	s_mov_b64 s[6:7], -1
	v_add_f32_e32 v57, 1.0, v58
	v_rcp_f32_e32 v57, v57
	v_mul_f32_e32 v58, v4, v5
	v_mul_f32_e32 v4, v7, v15
	v_mul_f32_e32 v15, v6, v4
	v_mul_f32_e32 v4, v9, v57
	v_mul_f32_e32 v57, v8, v4
	v_pk_mul_f32 v[4:5], v[188:189], s[42:43] op_sel_hi:[1,0]
	v_mov_b32_e32 v6, v171
	v_mul_f32_e32 v7, 0xbfb8aa3b, v5
	v_exp_f32_e32 v8, v7
	v_cvt_pk_fp8_f32 v6, v10, v14
	v_mov_b32_e32 v7, v171
	v_cvt_pk_fp8_f32 v7, v13, v58
	v_add_f32_e32 v8, 1.0, v8
	v_rcp_f32_e32 v10, v8
	v_pk_mul_f32 v[8:9], v[116:117], s[42:43] op_sel_hi:[1,0]
	v_cvt_pk_fp8_f32 v6, v11, v56 op_sel:[0,0,1]
	v_mul_f32_e32 v11, 0xbfb8aa3b, v9
	v_exp_f32_e32 v11, v11
	v_mul_f32_e32 v5, v5, v10
	v_mul_f32_e32 v13, v4, v5
	v_cvt_pk_fp8_f32 v7, v15, v57 op_sel:[0,0,1]
	v_add_f32_e32 v4, 1.0, v11
	v_rcp_f32_e32 v14, v4
	v_pk_mul_f32 v[4:5], v[186:187], s[42:43] op_sel_hi:[1,0]
	s_andn2_b64 vcc, exec, s[2:3]
	v_mul_f32_e32 v10, 0xbfb8aa3b, v5
	v_exp_f32_e32 v15, v10
	v_pk_mul_f32 v[10:11], v[118:119], s[42:43] op_sel_hi:[1,0]
	v_mul_f32_e32 v9, v9, v14
	v_mul_f32_e32 v56, 0xbfb8aa3b, v11
	v_exp_f32_e32 v56, v56
	v_add_f32_e32 v14, 1.0, v15
	v_rcp_f32_e32 v14, v14
	s_mov_b32 s75, s74
	v_add_f32_e32 v15, 1.0, v56
	v_rcp_f32_e32 v15, v15
	v_mul_f32_e32 v5, v5, v14
	v_mul_f32_e32 v14, v4, v5
	v_pk_mul_f32 v[4:5], v[184:185], s[42:43] op_sel_hi:[1,0]
	v_mul_f32_e32 v56, v8, v9
	v_mul_f32_e32 v8, 0xbfb8aa3b, v5
	v_mul_f32_e32 v11, v11, v15
	v_exp_f32_e32 v15, v8
	v_pk_mul_f32 v[8:9], v[112:113], s[42:43] op_sel_hi:[1,0]
	v_mul_f32_e32 v58, v10, v11
	v_mul_f32_e32 v57, 0xbfb8aa3b, v9
	v_exp_f32_e32 v57, v57
	v_add_f32_e32 v10, 1.0, v15
	v_rcp_f32_e32 v15, v10
	s_mov_b32 s48, s44
	v_add_f32_e32 v10, 1.0, v57
	v_rcp_f32_e32 v57, v10
	v_pk_mul_f32 v[10:11], v[182:183], s[42:43] op_sel_hi:[1,0]
	v_mul_f32_e32 v5, v5, v15
	v_mul_f32_e32 v59, 0xbfb8aa3b, v11
	v_exp_f32_e32 v59, v59
	v_mul_f32_e32 v15, v4, v5
	v_mul_f32_e32 v9, v9, v57
	v_mul_f32_e32 v60, v8, v9
	v_add_f32_e32 v4, 1.0, v59
	v_rcp_f32_e32 v57, v4
	v_pk_mul_f32 v[4:5], v[114:115], s[42:43] op_sel_hi:[1,0]
	v_mov_b32_e32 v9, v171
	v_mul_f32_e32 v59, 0xbfb8aa3b, v5
	v_exp_f32_e32 v59, v59
	v_mul_f32_e32 v8, v11, v57
	v_mul_f32_e32 v10, v10, v8
	v_cvt_pk_fp8_f32 v9, v15, v60
	v_add_f32_e32 v8, 1.0, v59
	v_rcp_f32_e32 v11, v8
	v_mov_b32_e32 v8, v171
	v_cvt_pk_fp8_f32 v8, v13, v56
	v_pk_mul_f32 v[56:57], v[110:111], s[42:43] op_sel_hi:[1,0]
	v_mul_f32_e32 v5, v5, v11
	v_mul_f32_e32 v4, v4, v5
	v_cvt_pk_fp8_f32 v9, v10, v4 op_sel:[0,0,1]
	v_add3_u32 v4, s63, v12, v3
	v_ashrrev_i32_e32 v3, 31, v2
	v_pk_mul_f32 v[12:13], v[180:181], s[42:43] op_sel_hi:[1,0]
	v_lshlrev_b64 v[10:11], 9, v[2:3]
	v_mul_f32_e32 v3, 0xbfb8aa3b, v13
	v_cvt_pk_fp8_f32 v8, v14, v58 op_sel:[0,0,1]
	v_exp_f32_e32 v3, v3
	v_pk_mul_f32 v[14:15], v[108:109], s[42:43] op_sel_hi:[1,0]
	v_mul_f32_e32 v58, 0xbfb8aa3b, v57
	v_mul_f32_e32 v5, 0xbfb8aa3b, v15
	v_exp_f32_e32 v5, v5
	v_add_f32_e32 v3, 1.0, v3
	v_rcp_f32_e32 v3, v3
	v_exp_f32_e32 v58, v58
	v_add_f32_e32 v5, 1.0, v5
	v_rcp_f32_e32 v5, v5
	v_mul_f32_e32 v3, v13, v3
	v_mul_f32_e32 v3, v12, v3
	v_pk_mul_f32 v[12:13], v[178:179], s[42:43] op_sel_hi:[1,0]
	v_mul_f32_e32 v5, v15, v5
	v_mul_f32_e32 v15, 0xbfb8aa3b, v13
	v_exp_f32_e32 v15, v15
	v_mul_f32_e32 v5, v14, v5
	ds_write_b64 v4, v[6:7]
	ds_write_b64 v4, v[8:9] offset:768
	ds_read_b128 v[6:9], v1
	v_add_f32_e32 v14, 1.0, v15
	v_rcp_f32_e32 v59, v14
	v_add_f32_e32 v14, 1.0, v58
	v_rcp_f32_e32 v58, v14
	v_pk_mul_f32 v[14:15], v[176:177], s[42:43] op_sel_hi:[1,0]
	v_mul_f32_e32 v13, v13, v59
	v_mul_f32_e32 v60, 0xbfb8aa3b, v15
	v_exp_f32_e32 v60, v60
	v_mul_f32_e32 v59, v12, v13
	v_mul_f32_e32 v57, v57, v58
	v_mul_f32_e32 v61, v56, v57
	v_add_f32_e32 v12, 1.0, v60
	v_rcp_f32_e32 v58, v12
	v_pk_mul_f32 v[12:13], v[104:105], s[42:43] op_sel_hi:[1,0]
	v_lshl_add_u64 v[10:11], s[24:25], 0, v[10:11]
	v_mul_f32_e32 v60, 0xbfb8aa3b, v13
	v_exp_f32_e32 v60, v60
	v_mul_f32_e32 v15, v15, v58
	v_mul_f32_e32 v58, v14, v15
	v_lshl_add_u64 v[10:11], v[10:11], 0, s[4:5]
	v_add_f32_e32 v14, 1.0, v60
	v_rcp_f32_e32 v60, v14
	v_pk_mul_f32 v[14:15], v[174:175], s[42:43] op_sel_hi:[1,0]
	v_lshl_add_u64 v[10:11], v[10:11], 0, s[22:23]
	v_mul_f32_e32 v56, 0xbfb8aa3b, v15
	v_exp_f32_e32 v62, v56
	v_pk_mul_f32 v[56:57], v[106:107], s[42:43] op_sel_hi:[1,0]
	v_mul_f32_e32 v13, v13, v60
	v_mul_f32_e32 v63, 0xbfb8aa3b, v57
	v_exp_f32_e32 v63, v63
	v_add_f32_e32 v60, 1.0, v62
	v_rcp_f32_e32 v60, v60
	v_lshl_add_u64 v[10:11], v[10:11], 0, v[170:171]
	v_add_f32_e32 v62, 1.0, v63
	v_rcp_f32_e32 v62, v62
	v_mul_f32_e32 v63, v12, v13
	v_mul_f32_e32 v12, v15, v60
	v_mul_f32_e32 v60, v14, v12
	v_mul_f32_e32 v12, v57, v62
	v_mul_f32_e32 v56, v56, v12
	v_mov_b32_e32 v12, v171
	v_pk_mul_f32 v[14:15], v[54:55], s[42:43] op_sel_hi:[1,0]
	v_cvt_pk_fp8_f32 v12, v3, v5
	v_mul_f32_e32 v3, 0xbfb8aa3b, v15
	v_exp_f32_e32 v3, v3
	v_pk_mul_f32 v[54:55], v[96:97], s[42:43] op_sel_hi:[1,0]
	v_mov_b32_e32 v13, v171
	v_mul_f32_e32 v5, 0xbfb8aa3b, v55
	v_add_f32_e32 v3, 1.0, v3
	v_rcp_f32_e32 v3, v3
	v_exp_f32_e32 v5, v5
	v_cvt_pk_fp8_f32 v13, v58, v63
	v_cvt_pk_fp8_f32 v12, v59, v61 op_sel:[0,0,1]
	v_mul_f32_e32 v3, v15, v3
	v_mul_f32_e32 v3, v14, v3
	v_pk_mul_f32 v[14:15], v[50:51], s[42:43] op_sel_hi:[1,0]
	v_add_f32_e32 v5, 1.0, v5
	v_mul_f32_e32 v50, 0xbfb8aa3b, v15
	v_cvt_pk_fp8_f32 v13, v60, v56 op_sel:[0,0,1]
	v_rcp_f32_e32 v5, v5
	v_exp_f32_e32 v56, v50
	v_pk_mul_f32 v[50:51], v[98:99], s[42:43] op_sel_hi:[1,0]
	s_waitcnt lgkmcnt(0)
	global_store_dwordx4 v[10:11], v[6:9], off
	v_mul_f32_e32 v57, 0xbfb8aa3b, v51
	v_exp_f32_e32 v57, v57
	v_mul_f32_e32 v5, v55, v5
	v_add_f32_e32 v55, 1.0, v56
	v_rcp_f32_e32 v55, v55
	v_add_f32_e32 v56, 1.0, v57
	v_rcp_f32_e32 v56, v56
	v_mul_f32_e32 v5, v54, v5
	v_mul_f32_e32 v15, v15, v55
	v_mul_f32_e32 v54, v14, v15
	v_pk_mul_f32 v[14:15], v[44:45], s[42:43] op_sel_hi:[1,0]
	v_mul_f32_e32 v51, v51, v56
	v_mul_f32_e32 v44, 0xbfb8aa3b, v15
	v_exp_f32_e32 v55, v44
	v_pk_mul_f32 v[44:45], v[88:89], s[42:43] op_sel_hi:[1,0]
	v_mul_f32_e32 v50, v50, v51
	v_mul_f32_e32 v56, 0xbfb8aa3b, v45
	v_exp_f32_e32 v56, v56
	v_add_f32_e32 v51, 1.0, v55
	v_rcp_f32_e32 v51, v51
	v_add_u32_e32 v10, 32, v2
	v_add_f32_e32 v55, 1.0, v56
	v_mul_f32_e32 v56, 0xbfb8aa3b, v43
	v_exp_f32_e32 v56, v56
	v_rcp_f32_e32 v55, v55
	v_mul_f32_e32 v15, v15, v51
	v_mul_f32_e32 v51, v14, v15
	v_add_f32_e32 v14, 1.0, v56
	v_mul_f32_e32 v45, v45, v55
	v_rcp_f32_e32 v55, v14
	v_pk_mul_f32 v[14:15], v[90:91], s[42:43] op_sel_hi:[1,0]
	v_mul_f32_e32 v44, v44, v45
	v_mul_f32_e32 v56, 0xbfb8aa3b, v15
	v_exp_f32_e32 v56, v56
	v_mul_f32_e32 v43, v43, v55
	v_mul_f32_e32 v45, v42, v43
	v_mov_b32_e32 v43, v171
	v_add_f32_e32 v42, 1.0, v56
	v_rcp_f32_e32 v55, v42
	v_mov_b32_e32 v42, v171
	v_cvt_pk_fp8_f32 v42, v3, v5
	v_cvt_pk_fp8_f32 v43, v51, v44
	v_mul_f32_e32 v3, v15, v55
	v_mul_f32_e32 v3, v14, v3
	v_cvt_pk_fp8_f32 v42, v54, v50 op_sel:[0,0,1]
	v_cvt_pk_fp8_f32 v43, v45, v3 op_sel:[0,0,1]
	ds_write_b64 v4, v[12:13]
	ds_write_b64 v4, v[42:43] offset:768
	v_pk_mul_f32 v[12:13], v[52:53], s[42:43] op_sel_hi:[1,0]
	v_pk_mul_f32 v[14:15], v[100:101], s[42:43] op_sel_hi:[1,0]
	v_mul_f32_e32 v3, 0xbfb8aa3b, v13
	v_exp_f32_e32 v3, v3
	v_mul_f32_e32 v5, 0xbfb8aa3b, v15
	v_exp_f32_e32 v5, v5
	v_pk_mul_f32 v[42:43], v[102:103], s[42:43] op_sel_hi:[1,0]
	v_add_f32_e32 v3, 1.0, v3
	v_rcp_f32_e32 v3, v3
	v_add_f32_e32 v5, 1.0, v5
	v_rcp_f32_e32 v5, v5
	v_mul_f32_e32 v44, 0xbfb8aa3b, v43
	v_mul_f32_e32 v3, v13, v3
	v_mul_f32_e32 v3, v12, v3
	v_pk_mul_f32 v[12:13], v[48:49], s[42:43] op_sel_hi:[1,0]
	v_mul_f32_e32 v5, v15, v5
	v_mul_f32_e32 v15, 0xbfb8aa3b, v13
	v_exp_f32_e32 v15, v15
	v_exp_f32_e32 v44, v44
	v_mul_f32_e32 v5, v14, v5
	v_ashrrev_i32_e32 v11, 31, v10
	v_add_f32_e32 v14, 1.0, v15
	v_rcp_f32_e32 v45, v14
	v_add_f32_e32 v14, 1.0, v44
	v_rcp_f32_e32 v44, v14
	v_pk_mul_f32 v[14:15], v[46:47], s[42:43] op_sel_hi:[1,0]
	v_mul_f32_e32 v13, v13, v45
	v_mul_f32_e32 v46, 0xbfb8aa3b, v15
	v_exp_f32_e32 v46, v46
	v_mul_f32_e32 v45, v12, v13
	v_mul_f32_e32 v43, v43, v44
	v_mul_f32_e32 v42, v42, v43
	v_add_f32_e32 v12, 1.0, v46
	v_rcp_f32_e32 v44, v12
	v_pk_mul_f32 v[12:13], v[92:93], s[42:43] op_sel_hi:[1,0]
	ds_read_b128 v[6:9], v1
	v_mul_f32_e32 v46, 0xbfb8aa3b, v13
	v_exp_f32_e32 v46, v46
	v_mul_f32_e32 v15, v15, v44
	v_mul_f32_e32 v43, v14, v15
	v_lshlrev_b64 v[10:11], 9, v[10:11]
	v_add_f32_e32 v14, 1.0, v46
	v_rcp_f32_e32 v44, v14
	v_pk_mul_f32 v[14:15], v[40:41], s[42:43] op_sel_hi:[1,0]
	v_lshl_add_u64 v[10:11], s[24:25], 0, v[10:11]
	v_mul_f32_e32 v40, 0xbfb8aa3b, v15
	v_exp_f32_e32 v46, v40
	v_pk_mul_f32 v[40:41], v[94:95], s[42:43] op_sel_hi:[1,0]
	v_mul_f32_e32 v13, v13, v44
	v_mul_f32_e32 v47, 0xbfb8aa3b, v41
	v_exp_f32_e32 v47, v47
	v_add_f32_e32 v44, 1.0, v46
	v_rcp_f32_e32 v44, v44
	v_lshl_add_u64 v[10:11], v[10:11], 0, s[4:5]
	v_add_f32_e32 v46, 1.0, v47
	v_rcp_f32_e32 v46, v46
	v_mul_f32_e32 v47, v12, v13
	v_mul_f32_e32 v12, v15, v44
	v_mul_f32_e32 v44, v14, v12
	v_mul_f32_e32 v12, v41, v46
	v_mul_f32_e32 v40, v40, v12
	v_mov_b32_e32 v12, v171
	v_pk_mul_f32 v[14:15], v[38:39], s[42:43] op_sel_hi:[1,0]
	v_cvt_pk_fp8_f32 v12, v3, v5
	v_mul_f32_e32 v3, 0xbfb8aa3b, v15
	v_exp_f32_e32 v3, v3
	v_pk_mul_f32 v[38:39], v[84:85], s[42:43] op_sel_hi:[1,0]
	v_mov_b32_e32 v13, v171
	v_mul_f32_e32 v5, 0xbfb8aa3b, v39
	v_add_f32_e32 v3, 1.0, v3
	v_rcp_f32_e32 v3, v3
	v_exp_f32_e32 v5, v5
	v_cvt_pk_fp8_f32 v13, v43, v47
	v_cvt_pk_fp8_f32 v12, v45, v42 op_sel:[0,0,1]
	v_mul_f32_e32 v3, v15, v3
	v_mul_f32_e32 v3, v14, v3
	v_pk_mul_f32 v[14:15], v[36:37], s[42:43] op_sel_hi:[1,0]
	v_add_f32_e32 v5, 1.0, v5
	v_mul_f32_e32 v36, 0xbfb8aa3b, v15
	v_cvt_pk_fp8_f32 v13, v44, v40 op_sel:[0,0,1]
	v_rcp_f32_e32 v5, v5
	v_exp_f32_e32 v40, v36
	v_pk_mul_f32 v[36:37], v[86:87], s[42:43] op_sel_hi:[1,0]
	v_lshl_add_u64 v[10:11], v[10:11], 0, s[22:23]
	v_mul_f32_e32 v41, 0xbfb8aa3b, v37
	v_exp_f32_e32 v41, v41
	v_mul_f32_e32 v5, v39, v5
	v_add_f32_e32 v39, 1.0, v40
	v_rcp_f32_e32 v39, v39
	v_add_f32_e32 v40, 1.0, v41
	v_rcp_f32_e32 v40, v40
	v_mul_f32_e32 v5, v38, v5
	v_mul_f32_e32 v15, v15, v39
	v_mul_f32_e32 v38, v14, v15
	v_pk_mul_f32 v[14:15], v[34:35], s[42:43] op_sel_hi:[1,0]
	v_mul_f32_e32 v37, v37, v40
	v_mul_f32_e32 v34, 0xbfb8aa3b, v15
	v_exp_f32_e32 v39, v34
	v_pk_mul_f32 v[34:35], v[80:81], s[42:43] op_sel_hi:[1,0]
	v_mul_f32_e32 v36, v36, v37
	v_mul_f32_e32 v40, 0xbfb8aa3b, v35
	v_exp_f32_e32 v40, v40
	v_add_f32_e32 v37, 1.0, v39
	v_rcp_f32_e32 v37, v37
	v_lshl_add_u64 v[10:11], v[10:11], 0, v[170:171]
	v_add_f32_e32 v39, 1.0, v40
	v_mul_f32_e32 v40, 0xbfb8aa3b, v33
	v_exp_f32_e32 v40, v40
	v_rcp_f32_e32 v39, v39
	v_mul_f32_e32 v15, v15, v37
	v_mul_f32_e32 v37, v14, v15
	v_add_f32_e32 v14, 1.0, v40
	v_mul_f32_e32 v35, v35, v39
	v_rcp_f32_e32 v39, v14
	v_pk_mul_f32 v[14:15], v[82:83], s[42:43] op_sel_hi:[1,0]
	v_mul_f32_e32 v34, v34, v35
	v_mul_f32_e32 v40, 0xbfb8aa3b, v15
	v_exp_f32_e32 v40, v40
	v_mul_f32_e32 v33, v33, v39
	v_mul_f32_e32 v35, v32, v33
	v_mov_b32_e32 v33, v171
	v_add_f32_e32 v32, 1.0, v40
	v_rcp_f32_e32 v39, v32
	v_mov_b32_e32 v32, v171
	v_cvt_pk_fp8_f32 v32, v3, v5
	v_cvt_pk_fp8_f32 v33, v37, v34
	v_mul_f32_e32 v3, v15, v39
	v_mul_f32_e32 v3, v14, v3
	v_cvt_pk_fp8_f32 v32, v38, v36 op_sel:[0,0,1]
	v_cvt_pk_fp8_f32 v33, v35, v3 op_sel:[0,0,1]
	s_waitcnt lgkmcnt(0)
	global_store_dwordx4 v[10:11], v[6:9], off
	ds_write_b64 v4, v[12:13]
	ds_write_b64 v4, v[32:33] offset:768
	v_pk_mul_f32 v[12:13], v[30:31], s[42:43] op_sel_hi:[1,0]
	v_pk_mul_f32 v[14:15], v[76:77], s[42:43] op_sel_hi:[1,0]
	v_mul_f32_e32 v3, 0xbfb8aa3b, v13
	v_exp_f32_e32 v3, v3
	v_mul_f32_e32 v5, 0xbfb8aa3b, v15
	v_exp_f32_e32 v5, v5
	v_add_u32_e32 v10, 0x80, v2
	v_add_f32_e32 v3, 1.0, v3
	v_rcp_f32_e32 v3, v3
	v_add_f32_e32 v5, 1.0, v5
	v_rcp_f32_e32 v5, v5
	v_ashrrev_i32_e32 v11, 31, v10
	v_mul_f32_e32 v3, v13, v3
	v_mul_f32_e32 v3, v12, v3
	v_pk_mul_f32 v[12:13], v[28:29], s[42:43] op_sel_hi:[1,0]
	v_mul_f32_e32 v5, v15, v5
	v_mul_f32_e32 v15, 0xbfb8aa3b, v13
	v_pk_mul_f32 v[28:29], v[78:79], s[42:43] op_sel_hi:[1,0]
	v_exp_f32_e32 v15, v15
	v_mul_f32_e32 v30, 0xbfb8aa3b, v29
	v_exp_f32_e32 v30, v30
	v_mul_f32_e32 v5, v14, v5
	v_add_f32_e32 v14, 1.0, v15
	v_rcp_f32_e32 v31, v14
	v_add_f32_e32 v14, 1.0, v30
	v_rcp_f32_e32 v30, v14
	v_pk_mul_f32 v[14:15], v[26:27], s[42:43] op_sel_hi:[1,0]
	v_mul_f32_e32 v13, v13, v31
	v_mul_f32_e32 v26, 0xbfb8aa3b, v15
	v_exp_f32_e32 v26, v26
	v_mul_f32_e32 v27, v12, v13
	v_mul_f32_e32 v29, v29, v30
	v_mul_f32_e32 v28, v28, v29
	v_add_f32_e32 v12, 1.0, v26
	v_rcp_f32_e32 v26, v12
	v_pk_mul_f32 v[12:13], v[72:73], s[42:43] op_sel_hi:[1,0]
	ds_read_b128 v[6:9], v1
	v_mul_f32_e32 v30, 0xbfb8aa3b, v13
	v_exp_f32_e32 v30, v30
	v_mul_f32_e32 v15, v15, v26
	v_mul_f32_e32 v26, v14, v15
	v_lshlrev_b64 v[10:11], 9, v[10:11]
	v_add_f32_e32 v14, 1.0, v30
	v_rcp_f32_e32 v29, v14
	v_pk_mul_f32 v[14:15], v[24:25], s[42:43] op_sel_hi:[1,0]
	v_lshl_add_u64 v[10:11], s[24:25], 0, v[10:11]
	v_mul_f32_e32 v24, 0xbfb8aa3b, v15
	v_exp_f32_e32 v30, v24
	v_pk_mul_f32 v[24:25], v[74:75], s[42:43] op_sel_hi:[1,0]
	v_mul_f32_e32 v13, v13, v29
	v_mul_f32_e32 v31, 0xbfb8aa3b, v25
	v_exp_f32_e32 v31, v31
	v_add_f32_e32 v29, 1.0, v30
	v_rcp_f32_e32 v29, v29
	v_lshl_add_u64 v[10:11], v[10:11], 0, s[4:5]
	v_add_f32_e32 v30, 1.0, v31
	v_rcp_f32_e32 v30, v30
	v_mul_f32_e32 v31, v12, v13
	v_mul_f32_e32 v12, v15, v29
	v_mul_f32_e32 v29, v14, v12
	v_mul_f32_e32 v12, v25, v30
	v_mul_f32_e32 v24, v24, v12
	v_mov_b32_e32 v12, v171
	v_pk_mul_f32 v[14:15], v[22:23], s[42:43] op_sel_hi:[1,0]
	v_cvt_pk_fp8_f32 v12, v3, v5
	v_mul_f32_e32 v3, 0xbfb8aa3b, v15
	v_exp_f32_e32 v3, v3
	v_pk_mul_f32 v[22:23], v[68:69], s[42:43] op_sel_hi:[1,0]
	v_mov_b32_e32 v13, v171
	v_mul_f32_e32 v5, 0xbfb8aa3b, v23
	v_add_f32_e32 v3, 1.0, v3
	v_rcp_f32_e32 v3, v3
	v_exp_f32_e32 v5, v5
	v_cvt_pk_fp8_f32 v13, v26, v31
	v_cvt_pk_fp8_f32 v12, v27, v28 op_sel:[0,0,1]
	v_mul_f32_e32 v3, v15, v3
	v_mul_f32_e32 v3, v14, v3
	v_pk_mul_f32 v[14:15], v[20:21], s[42:43] op_sel_hi:[1,0]
	v_add_f32_e32 v5, 1.0, v5
	v_mul_f32_e32 v20, 0xbfb8aa3b, v15
	v_cvt_pk_fp8_f32 v13, v29, v24 op_sel:[0,0,1]
	v_rcp_f32_e32 v5, v5
	v_exp_f32_e32 v24, v20
	v_pk_mul_f32 v[20:21], v[70:71], s[42:43] op_sel_hi:[1,0]
	v_lshl_add_u64 v[10:11], v[10:11], 0, s[22:23]
	v_mul_f32_e32 v25, 0xbfb8aa3b, v21
	v_exp_f32_e32 v25, v25
	v_mul_f32_e32 v5, v23, v5
	v_add_f32_e32 v23, 1.0, v24
	v_rcp_f32_e32 v23, v23
	v_add_f32_e32 v24, 1.0, v25
	v_rcp_f32_e32 v24, v24
	v_mul_f32_e32 v5, v22, v5
	v_mul_f32_e32 v15, v15, v23
	v_mul_f32_e32 v22, v14, v15
	v_pk_mul_f32 v[14:15], v[18:19], s[42:43] op_sel_hi:[1,0]
	v_mul_f32_e32 v21, v21, v24
	v_mul_f32_e32 v18, 0xbfb8aa3b, v15
	v_exp_f32_e32 v23, v18
	v_pk_mul_f32 v[18:19], v[64:65], s[42:43] op_sel_hi:[1,0]
	v_mul_f32_e32 v20, v20, v21
	v_mul_f32_e32 v24, 0xbfb8aa3b, v19
	v_exp_f32_e32 v24, v24
	v_add_f32_e32 v21, 1.0, v23
	v_rcp_f32_e32 v21, v21
	v_lshl_add_u64 v[10:11], v[10:11], 0, v[170:171]
	v_add_f32_e32 v23, 1.0, v24
	v_mul_f32_e32 v24, 0xbfb8aa3b, v17
	v_exp_f32_e32 v24, v24
	v_rcp_f32_e32 v23, v23
	v_mul_f32_e32 v15, v15, v21
	v_mul_f32_e32 v21, v14, v15
	v_add_f32_e32 v14, 1.0, v24
	v_mul_f32_e32 v19, v19, v23
	v_rcp_f32_e32 v23, v14
	v_pk_mul_f32 v[14:15], v[66:67], s[42:43] op_sel_hi:[1,0]
	v_mul_f32_e32 v18, v18, v19
	v_mul_f32_e32 v24, 0xbfb8aa3b, v15
	v_exp_f32_e32 v24, v24
	v_mul_f32_e32 v17, v17, v23
	v_mul_f32_e32 v19, v16, v17
	v_mov_b32_e32 v17, v171
	v_add_f32_e32 v16, 1.0, v24
	v_rcp_f32_e32 v23, v16
	v_mov_b32_e32 v16, v171
	v_cvt_pk_fp8_f32 v16, v3, v5
	v_cvt_pk_fp8_f32 v17, v21, v18
	v_mul_f32_e32 v3, v15, v23
	v_mul_f32_e32 v3, v14, v3
	v_cvt_pk_fp8_f32 v16, v22, v20 op_sel:[0,0,1]
	v_cvt_pk_fp8_f32 v17, v19, v3 op_sel:[0,0,1]
	v_add_u32_e32 v2, 0xa0, v2
	s_waitcnt lgkmcnt(0)
	global_store_dwordx4 v[10:11], v[6:9], off
	ds_write_b64 v4, v[12:13]
	ds_write_b64 v4, v[16:17] offset:768
	v_ashrrev_i32_e32 v3, 31, v2
	ds_read_b128 v[4:7], v1
	v_lshlrev_b64 v[2:3], 9, v[2:3]
	v_lshl_add_u64 v[2:3], s[24:25], 0, v[2:3]
	v_lshl_add_u64 v[2:3], v[2:3], 0, s[4:5]
	v_lshl_add_u64 v[2:3], v[2:3], 0, s[22:23]
	v_lshl_add_u64 v[2:3], v[2:3], 0, v[170:171]
	s_mov_b64 s[50:51], s[46:47]
	v_mov_b32_e32 v181, v206
	v_mov_b32_e32 v180, v207
	v_mov_b32_e32 v174, v208
	v_mov_b32_e32 v175, v209
	s_waitcnt lgkmcnt(0)
	global_store_dwordx4 v[2:3], v[4:7], off
	s_cbranch_vccz .LBB0_1396

.LBB0_1473:
	v_mov_b32_e32 v19, v187
	v_mov_b32_e32 v17, v186
	s_nop 15
	s_nop 15
	v_pk_mul_f32 v[24:25], v[140:141], s[30:31] op_sel_hi:[1,0]
	v_lshl_add_u32 v18, v17, 4, v19
	v_ashrrev_i32_e32 v18, 2, v18
	v_and_b32_e32 v20, 3, v19
	v_mul_lo_u32 v21, v19, s71
	v_lshlrev_b32_e32 v17, 3, v17
	v_add3_u32 v17, s68, v21, v17
	v_mul_lo_u32 v21, v18, s71
	v_lshlrev_b32_e32 v20, 4, v20
	v_add3_u32 v22, s68, v21, v20
	v_lshlrev_b32_e32 v20, 6, v19
	v_and_b32_e32 v180, 0x80, v20
	v_pk_mul_f32 v[20:21], v[136:137], s[30:31] op_sel_hi:[1,0]
	v_mov_b32_e32 v26, v181
	v_mov_b32_e32 v27, v181
	v_cvt_pk_fp8_f32 v26, v20, v21
	v_cvt_pk_fp8_f32 v27, v24, v25
	v_pk_mul_f32 v[20:21], v[138:139], s[30:31] op_sel_hi:[1,0]
	v_pk_mul_f32 v[24:25], v[142:143], s[30:31] op_sel_hi:[1,0]
	v_cvt_pk_fp8_f32 v26, v20, v21 op_sel:[0,0,1]
	v_cvt_pk_fp8_f32 v27, v24, v25 op_sel:[0,0,1]
	v_pk_mul_f32 v[20:21], v[160:161], s[30:31] op_sel_hi:[1,0]
	v_pk_mul_f32 v[24:25], v[164:165], s[30:31] op_sel_hi:[1,0]
	v_mov_b32_e32 v28, v181
	v_mov_b32_e32 v29, v181
	v_cvt_pk_fp8_f32 v28, v20, v21
	v_cvt_pk_fp8_f32 v29, v24, v25
	v_pk_mul_f32 v[30:31], v[120:121], s[30:31] op_sel_hi:[1,0]
	v_pk_mul_f32 v[32:33], v[124:125], s[30:31] op_sel_hi:[1,0]
	v_mov_b32_e32 v34, v181
	v_mov_b32_e32 v35, v181
	v_cvt_pk_fp8_f32 v34, v30, v31
	v_cvt_pk_fp8_f32 v35, v32, v33
	s_lshl_b32 s6, s42, 8
	v_pk_mul_f32 v[20:21], v[162:163], s[30:31] op_sel_hi:[1,0]
	v_pk_mul_f32 v[24:25], v[166:167], s[30:31] op_sel_hi:[1,0]
	s_add_i32 s6, s6, s65
	v_cvt_pk_fp8_f32 v28, v20, v21 op_sel:[0,0,1]
	v_cvt_pk_fp8_f32 v29, v24, v25 op_sel:[0,0,1]
	v_pk_mul_f32 v[30:31], v[122:123], s[30:31] op_sel_hi:[1,0]
	v_pk_mul_f32 v[32:33], v[126:127], s[30:31] op_sel_hi:[1,0]
	v_add_u32_e32 v18, s6, v18
	v_lshlrev_b32_e32 v19, 4, v19
	v_cvt_pk_fp8_f32 v34, v30, v31 op_sel:[0,0,1]
	v_cvt_pk_fp8_f32 v35, v32, v33 op_sel:[0,0,1]
	v_pk_mul_f32 v[30:31], v[144:145], s[30:31] op_sel_hi:[1,0]
	v_pk_mul_f32 v[32:33], v[152:153], s[30:31] op_sel_hi:[1,0]
	v_mov_b32_e32 v36, v181
	v_mov_b32_e32 v37, v181
	v_and_b32_e32 v20, 16, v19
	v_ashrrev_i32_e32 v19, 31, v18
	v_cvt_pk_fp8_f32 v36, v30, v31
	v_cvt_pk_fp8_f32 v37, v32, v33
	s_lshl_b32 s6, s44, 8
	ds_write_b64 v17, v[26:27]
	ds_write_b64 v17, v[28:29] offset:32
	v_lshlrev_b64 v[28:29], 11, v[18:19]
	s_ashr_i32 s7, s6, 31
	ds_read_b128 v[24:27], v22
	v_lshl_add_u64 v[28:29], s[20:21], 0, v[28:29]
	v_lshl_add_u64 v[28:29], v[28:29], 0, s[6:7]
	v_pk_mul_f32 v[30:31], v[146:147], s[30:31] op_sel_hi:[1,0]
	v_pk_mul_f32 v[32:33], v[154:155], s[30:31] op_sel_hi:[1,0]
	v_lshl_add_u64 v[28:29], v[28:29], 0, v[180:181]
	v_cvt_pk_fp8_f32 v36, v30, v31 op_sel:[0,0,1]
	v_cvt_pk_fp8_f32 v37, v32, v33 op_sel:[0,0,1]
	v_mov_b32_e32 v21, v181
	v_lshl_add_u64 v[28:29], v[28:29], 0, s[18:19]
	v_lshl_add_u64 v[28:29], v[28:29], 0, v[20:21]
	s_waitcnt lgkmcnt(0)
	global_store_dwordx4 v[28:29], v[24:27], off
	ds_write_b64 v17, v[34:35]
	ds_write_b64 v17, v[36:37] offset:32
	v_pk_mul_f32 v[30:31], v[96:97], s[30:31] op_sel_hi:[1,0]
	v_pk_mul_f32 v[32:33], v[100:101], s[30:31] op_sel_hi:[1,0]
	v_mov_b32_e32 v34, v181
	v_mov_b32_e32 v35, v181
	v_cvt_pk_fp8_f32 v34, v30, v31
	v_cvt_pk_fp8_f32 v35, v32, v33
	v_pk_mul_f32 v[30:31], v[98:99], s[30:31] op_sel_hi:[1,0]
	v_pk_mul_f32 v[32:33], v[102:103], s[30:31] op_sel_hi:[1,0]
	v_add_u32_e32 v28, 16, v18
	v_cvt_pk_fp8_f32 v34, v30, v31 op_sel:[0,0,1]
	v_cvt_pk_fp8_f32 v35, v32, v33 op_sel:[0,0,1]
	v_pk_mul_f32 v[30:31], v[128:129], s[30:31] op_sel_hi:[1,0]
	v_pk_mul_f32 v[32:33], v[132:133], s[30:31] op_sel_hi:[1,0]
	v_mov_b32_e32 v36, v181
	v_mov_b32_e32 v37, v181
	v_ashrrev_i32_e32 v29, 31, v28
	v_cvt_pk_fp8_f32 v36, v30, v31
	v_cvt_pk_fp8_f32 v37, v32, v33
	v_lshlrev_b64 v[28:29], 11, v[28:29]
	ds_read_b128 v[24:27], v22
	v_lshl_add_u64 v[28:29], s[20:21], 0, v[28:29]
	v_lshl_add_u64 v[28:29], v[28:29], 0, s[6:7]
	v_pk_mul_f32 v[30:31], v[130:131], s[30:31] op_sel_hi:[1,0]
	v_pk_mul_f32 v[32:33], v[134:135], s[30:31] op_sel_hi:[1,0]
	v_lshl_add_u64 v[28:29], v[28:29], 0, v[180:181]
	v_cvt_pk_fp8_f32 v36, v30, v31 op_sel:[0,0,1]
	v_cvt_pk_fp8_f32 v37, v32, v33 op_sel:[0,0,1]
	v_lshl_add_u64 v[28:29], v[28:29], 0, s[18:19]
	v_lshl_add_u64 v[28:29], v[28:29], 0, v[20:21]
	s_waitcnt lgkmcnt(0)
	global_store_dwordx4 v[28:29], v[24:27], off
	ds_write_b64 v17, v[34:35]
	ds_write_b64 v17, v[36:37] offset:32
	v_pk_mul_f32 v[30:31], v[80:81], s[30:31] op_sel_hi:[1,0]
	v_pk_mul_f32 v[32:33], v[84:85], s[30:31] op_sel_hi:[1,0]
	v_mov_b32_e32 v34, v181
	v_mov_b32_e32 v35, v181
	v_cvt_pk_fp8_f32 v34, v30, v31
	v_cvt_pk_fp8_f32 v35, v32, v33
	v_pk_mul_f32 v[30:31], v[82:83], s[30:31] op_sel_hi:[1,0]
	v_pk_mul_f32 v[32:33], v[86:87], s[30:31] op_sel_hi:[1,0]
	v_add_u32_e32 v28, 32, v18
	v_cvt_pk_fp8_f32 v34, v30, v31 op_sel:[0,0,1]
	v_cvt_pk_fp8_f32 v35, v32, v33 op_sel:[0,0,1]
	v_pk_mul_f32 v[30:31], v[104:105], s[30:31] op_sel_hi:[1,0]
	v_pk_mul_f32 v[32:33], v[112:113], s[30:31] op_sel_hi:[1,0]
	v_mov_b32_e32 v36, v181
	v_mov_b32_e32 v37, v181
	v_ashrrev_i32_e32 v29, 31, v28
	v_cvt_pk_fp8_f32 v36, v30, v31
	v_cvt_pk_fp8_f32 v37, v32, v33
	v_lshlrev_b64 v[28:29], 11, v[28:29]
	ds_read_b128 v[24:27], v22
	v_lshl_add_u64 v[28:29], s[20:21], 0, v[28:29]
	v_lshl_add_u64 v[28:29], v[28:29], 0, s[6:7]
	v_pk_mul_f32 v[30:31], v[106:107], s[30:31] op_sel_hi:[1,0]
	v_pk_mul_f32 v[32:33], v[114:115], s[30:31] op_sel_hi:[1,0]
	v_lshl_add_u64 v[28:29], v[28:29], 0, v[180:181]
	v_cvt_pk_fp8_f32 v36, v30, v31 op_sel:[0,0,1]
	v_cvt_pk_fp8_f32 v37, v32, v33 op_sel:[0,0,1]
	v_lshl_add_u64 v[28:29], v[28:29], 0, s[18:19]
	v_lshl_add_u64 v[28:29], v[28:29], 0, v[20:21]
	s_waitcnt lgkmcnt(0)
	global_store_dwordx4 v[28:29], v[24:27], off
	ds_write_b64 v17, v[34:35]
	ds_write_b64 v17, v[36:37] offset:32
	v_pk_mul_f32 v[30:31], v[108:109], s[30:31] op_sel_hi:[1,0]
	v_pk_mul_f32 v[32:33], v[116:117], s[30:31] op_sel_hi:[1,0]
	v_mov_b32_e32 v34, v181
	v_mov_b32_e32 v35, v181
	v_cvt_pk_fp8_f32 v34, v30, v31
	v_cvt_pk_fp8_f32 v35, v32, v33
	v_pk_mul_f32 v[30:31], v[110:111], s[30:31] op_sel_hi:[1,0]
	v_pk_mul_f32 v[32:33], v[118:119], s[30:31] op_sel_hi:[1,0]
	v_add_u32_e32 v28, 48, v18
	v_cvt_pk_fp8_f32 v34, v30, v31 op_sel:[0,0,1]
	v_cvt_pk_fp8_f32 v35, v32, v33 op_sel:[0,0,1]
	v_pk_mul_f32 v[30:31], v[148:149], s[30:31] op_sel_hi:[1,0]
	v_pk_mul_f32 v[32:33], v[156:157], s[30:31] op_sel_hi:[1,0]
	v_mov_b32_e32 v36, v181
	v_mov_b32_e32 v37, v181
	v_ashrrev_i32_e32 v29, 31, v28
	v_cvt_pk_fp8_f32 v36, v30, v31
	v_cvt_pk_fp8_f32 v37, v32, v33
	v_lshlrev_b64 v[28:29], 11, v[28:29]
	ds_read_b128 v[24:27], v22
	v_lshl_add_u64 v[28:29], s[20:21], 0, v[28:29]
	v_lshl_add_u64 v[28:29], v[28:29], 0, s[6:7]
	v_pk_mul_f32 v[30:31], v[150:151], s[30:31] op_sel_hi:[1,0]
	v_pk_mul_f32 v[32:33], v[158:159], s[30:31] op_sel_hi:[1,0]
	v_lshl_add_u64 v[28:29], v[28:29], 0, v[180:181]
	v_cvt_pk_fp8_f32 v36, v30, v31 op_sel:[0,0,1]
	v_cvt_pk_fp8_f32 v37, v32, v33 op_sel:[0,0,1]
	v_lshl_add_u64 v[28:29], v[28:29], 0, s[18:19]
	v_lshl_add_u64 v[28:29], v[28:29], 0, v[20:21]
	s_waitcnt lgkmcnt(0)
	global_store_dwordx4 v[28:29], v[24:27], off
	ds_write_b64 v17, v[34:35]
	ds_write_b64 v17, v[36:37] offset:32
	v_pk_mul_f32 v[30:31], v[88:89], s[30:31] op_sel_hi:[1,0]
	v_pk_mul_f32 v[32:33], v[92:93], s[30:31] op_sel_hi:[1,0]
	v_mov_b32_e32 v34, v181
	v_mov_b32_e32 v35, v181
	v_cvt_pk_fp8_f32 v34, v30, v31
	v_cvt_pk_fp8_f32 v35, v32, v33
	v_pk_mul_f32 v[30:31], v[90:91], s[30:31] op_sel_hi:[1,0]
	v_pk_mul_f32 v[32:33], v[94:95], s[30:31] op_sel_hi:[1,0]
	v_add_u32_e32 v28, 0x80, v18
	v_cvt_pk_fp8_f32 v34, v30, v31 op_sel:[0,0,1]
	v_cvt_pk_fp8_f32 v35, v32, v33 op_sel:[0,0,1]
	v_pk_mul_f32 v[30:31], v[56:57], s[30:31] op_sel_hi:[1,0]
	v_pk_mul_f32 v[32:33], v[60:61], s[30:31] op_sel_hi:[1,0]
	v_mov_b32_e32 v36, v181
	v_mov_b32_e32 v37, v181
	v_ashrrev_i32_e32 v29, 31, v28
	v_cvt_pk_fp8_f32 v36, v30, v31
	v_cvt_pk_fp8_f32 v37, v32, v33
	v_lshlrev_b64 v[28:29], 11, v[28:29]
	ds_read_b128 v[24:27], v22
	v_lshl_add_u64 v[28:29], s[20:21], 0, v[28:29]
	v_lshl_add_u64 v[28:29], v[28:29], 0, s[6:7]
	v_pk_mul_f32 v[30:31], v[58:59], s[30:31] op_sel_hi:[1,0]
	v_pk_mul_f32 v[32:33], v[62:63], s[30:31] op_sel_hi:[1,0]
	v_lshl_add_u64 v[28:29], v[28:29], 0, v[180:181]
	v_cvt_pk_fp8_f32 v36, v30, v31 op_sel:[0,0,1]
	v_cvt_pk_fp8_f32 v37, v32, v33 op_sel:[0,0,1]
	v_lshl_add_u64 v[28:29], v[28:29], 0, s[18:19]
	v_lshl_add_u64 v[28:29], v[28:29], 0, v[20:21]
	s_waitcnt lgkmcnt(0)
	global_store_dwordx4 v[28:29], v[24:27], off
	ds_write_b64 v17, v[34:35]
	ds_write_b64 v17, v[36:37] offset:32
	v_pk_mul_f32 v[30:31], v[72:73], s[30:31] op_sel_hi:[1,0]
	v_mov_b32_e32 v34, v181
	v_cvt_pk_fp8_f32 v34, v30, v31
	v_add_u32_e32 v28, 0x90, v18
	v_ashrrev_i32_e32 v29, 31, v28
	v_pk_mul_f32 v[30:31], v[74:75], s[30:31] op_sel_hi:[1,0]
	v_lshlrev_b64 v[28:29], 11, v[28:29]
	v_cvt_pk_fp8_f32 v34, v30, v31 op_sel:[0,0,1]
	v_pk_mul_f32 v[8:9], v[8:9], s[30:31] op_sel_hi:[1,0]
	v_mov_b32_e32 v30, v181
	ds_read_b128 v[24:27], v22
	v_lshl_add_u64 v[28:29], s[20:21], 0, v[28:29]
	v_cvt_pk_fp8_f32 v30, v8, v9
	v_lshl_add_u64 v[28:29], v[28:29], 0, s[6:7]
	v_lshl_add_u64 v[28:29], v[28:29], 0, v[180:181]
	v_lshl_add_u64 v[28:29], v[28:29], 0, s[18:19]
	v_pk_mul_f32 v[32:33], v[76:77], s[30:31] op_sel_hi:[1,0]
	v_mov_b32_e32 v35, v181
	v_pk_mul_f32 v[8:9], v[10:11], s[30:31] op_sel_hi:[1,0]
	v_cvt_pk_fp8_f32 v35, v32, v33
	v_pk_mul_f32 v[12:13], v[12:13], s[30:31] op_sel_hi:[1,0]
	v_mov_b32_e32 v31, v181
	v_cvt_pk_fp8_f32 v30, v8, v9 op_sel:[0,0,1]
	v_lshl_add_u64 v[8:9], v[28:29], 0, v[20:21]
	v_cvt_pk_fp8_f32 v31, v12, v13
	v_pk_mul_f32 v[10:11], v[14:15], s[30:31] op_sel_hi:[1,0]
	s_waitcnt lgkmcnt(0)
	global_store_dwordx4 v[8:9], v[24:27], off
	v_pk_mul_f32 v[14:15], v[68:69], s[30:31] op_sel_hi:[1,0]
	v_pk_mul_f32 v[32:33], v[78:79], s[30:31] op_sel_hi:[1,0]
	v_mov_b32_e32 v26, v181
	v_cvt_pk_fp8_f32 v26, v14, v15
	v_cvt_pk_fp8_f32 v35, v32, v33 op_sel:[0,0,1]
	v_cvt_pk_fp8_f32 v31, v10, v11 op_sel:[0,0,1]
	v_pk_mul_f32 v[24:25], v[64:65], s[30:31] op_sel_hi:[1,0]
	v_mov_b32_e32 v27, v181
	v_pk_mul_f32 v[14:15], v[70:71], s[30:31] op_sel_hi:[1,0]
	v_add_u32_e32 v12, 0xa0, v18
	v_cvt_pk_fp8_f32 v27, v24, v25
	v_cvt_pk_fp8_f32 v26, v14, v15 op_sel:[0,0,1]
	v_pk_mul_f32 v[4:5], v[4:5], s[30:31] op_sel_hi:[1,0]
	v_pk_mul_f32 v[0:1], v[0:1], s[30:31] op_sel_hi:[1,0]
	v_mov_b32_e32 v14, v181
	v_mov_b32_e32 v15, v181
	v_ashrrev_i32_e32 v13, 31, v12
	v_cvt_pk_fp8_f32 v14, v4, v5
	v_cvt_pk_fp8_f32 v15, v0, v1
	ds_write_b64 v17, v[34:35]
	ds_write_b64 v17, v[30:31] offset:32
	v_lshlrev_b64 v[12:13], 11, v[12:13]
	ds_read_b128 v[8:11], v22
	v_lshl_add_u64 v[12:13], s[20:21], 0, v[12:13]
	v_pk_mul_f32 v[24:25], v[66:67], s[30:31] op_sel_hi:[1,0]
	v_lshl_add_u64 v[12:13], v[12:13], 0, s[6:7]
	v_cvt_pk_fp8_f32 v27, v24, v25 op_sel:[0,0,1]
	v_pk_mul_f32 v[0:1], v[6:7], s[30:31] op_sel_hi:[1,0]
	v_pk_mul_f32 v[2:3], v[2:3], s[30:31] op_sel_hi:[1,0]
	v_lshl_add_u64 v[12:13], v[12:13], 0, v[180:181]
	v_cvt_pk_fp8_f32 v14, v0, v1 op_sel:[0,0,1]
	v_cvt_pk_fp8_f32 v15, v2, v3 op_sel:[0,0,1]
	v_lshl_add_u64 v[12:13], v[12:13], 0, s[18:19]
	v_add_u32_e32 v4, 0xb0, v18
	v_lshl_add_u64 v[0:1], v[12:13], 0, v[20:21]
	v_ashrrev_i32_e32 v5, 31, v4
	s_waitcnt lgkmcnt(0)
	global_store_dwordx4 v[0:1], v[8:11], off
	ds_write_b64 v17, v[26:27]
	ds_write_b64 v17, v[14:15] offset:32
	v_lshlrev_b64 v[4:5], 11, v[4:5]
	ds_read_b128 v[0:3], v22
	v_lshl_add_u64 v[4:5], s[20:21], 0, v[4:5]
	v_lshl_add_u64 v[4:5], v[4:5], 0, s[6:7]
	v_lshl_add_u64 v[4:5], v[4:5], 0, v[180:181]
	v_lshl_add_u64 v[4:5], v[4:5], 0, s[18:19]
	v_lshl_add_u64 v[4:5], v[4:5], 0, v[20:21]
	s_mov_b64 s[6:7], -1
	s_andn2_b64 vcc, exec, s[4:5]
	s_mov_b32 s44, s36
	s_mov_b32 s42, s34
	s_mov_b64 s[48:49], s[40:41]
	s_mov_b64 s[50:51], s[38:39]
	s_waitcnt lgkmcnt(0)
	global_store_dwordx4 v[4:5], v[0:3], off
	s_cbranch_vccz .LBB0_1488

.LBB0_1629:
	v_mov_b32_e32 v16, v189
	v_mov_b32_e32 v17, v188
	s_lshl_b32 s4, s54, 8
	s_nop 15
	s_nop 15
	s_add_i32 s4, s4, s73
	v_lshlrev_b32_e32 v18, 4, v17
	v_add_u32_e32 v28, s4, v16
	v_add_u32_e32 v19, v18, v16
	v_and_b32_e32 v33, 3, v16
	v_mul_lo_u32 v16, v16, s78
	v_ashrrev_i32_e32 v19, 2, v19
	v_add_u32_e32 v16, s76, v16
	v_add_u32_e32 v32, v16, v18
	v_mul_lo_u32 v16, v19, s78
	v_add_u32_e32 v16, s76, v16
	v_lshlrev_b32_e32 v178, 4, v33
	v_lshlrev_b32_e32 v26, 3, v17
	v_add_u32_e32 v30, s4, v19
	v_add_u32_e32 v25, v16, v178
	v_cmp_gt_i32_e32 vcc, 2, v17
	v_pk_mul_f32 v[18:19], v[146:147], s[34:35] op_sel_hi:[1,0]
	v_pk_mul_f32 v[16:17], v[144:145], s[34:35] op_sel_hi:[1,0]
	v_pk_mul_f32 v[20:21], v[150:151], s[34:35] op_sel_hi:[1,0]
	v_pk_mul_f32 v[22:23], v[148:149], s[34:35] op_sel_hi:[1,0]
	v_cvt_pk_bf16_f32 v16, v16, v17
	v_cvt_pk_bf16_f32 v17, v18, v19
	v_cvt_pk_bf16_f32 v18, v22, v23
	v_cvt_pk_bf16_f32 v19, v20, v21
	ds_write_b128 v32, v[16:19]
	v_pk_mul_f32 v[18:19], v[162:163], s[34:35] op_sel_hi:[1,0]
	v_pk_mul_f32 v[16:17], v[160:161], s[34:35] op_sel_hi:[1,0]
	v_pk_mul_f32 v[22:23], v[166:167], s[34:35] op_sel_hi:[1,0]
	v_pk_mul_f32 v[20:21], v[164:165], s[34:35] op_sel_hi:[1,0]
	v_cvt_pk_bf16_f32 v34, v16, v17
	v_cvt_pk_bf16_f32 v35, v18, v19
	v_cvt_pk_bf16_f32 v36, v20, v21
	v_cvt_pk_bf16_f32 v37, v22, v23
	v_ashrrev_i32_e32 v31, 31, v30
	s_lshl_b32 s4, s52, 8
	ds_write_b128 v32, v[34:37] offset:64
	v_lshlrev_b64 v[34:35], 13, v[30:31]
	s_ashr_i32 s5, s4, 31
	v_lshl_add_u64 v[42:43], s[14:15], 0, v[34:35]
	ds_read_b128 v[34:37], v25
	ds_read_b128 v[38:41], v25 offset:64
	s_cmp_eq_u32 s52, 15
	s_cselect_b64 s[6:7], -1, 0
	v_lshl_add_u64 v[42:43], s[4:5], 1, v[42:43]
	s_and_b64 s[6:7], s[30:31], s[6:7]
	v_lshl_add_u64 v[42:43], v[42:43], 0, s[12:13]
	s_and_b64 s[6:7], s[6:7], vcc
	v_ashrrev_i32_e32 v27, 31, v26
	v_lshl_add_u64 v[42:43], v[42:43], 0, v[178:179]
	v_ashrrev_i32_e32 v29, 31, v28
	s_waitcnt lgkmcnt(0)
	global_store_dwordx4 v[42:43], v[34:37], off
	global_store_dwordx4 v[42:43], v[38:41], off offset:256
	s_and_saveexec_b64 s[28:29], s[6:7]
	s_cbranch_execz .LBB0_1631
	v_lshlrev_b64 v[34:35], 6, v[28:29]
	v_lshl_add_u64 v[34:35], s[18:19], 0, v[34:35]
	v_lshl_add_u64 v[34:35], v[26:27], 2, v[34:35]
	global_store_dwordx4 v[34:35], v[16:19], off
	global_store_dwordx4 v[34:35], v[20:23], off offset:16

.LBB0_2391:
	v_mov_b32_e32 v17, v189
	v_mov_b32_e32 v19, v190
	s_nop 15
	s_nop 15
	s_lshl_b32 s4, s44, 8
	v_lshlrev_b32_e32 v17, 4, v17
	v_add_u32_e32 v18, v17, v19
	s_add_i32 s4, s4, s63
	v_ashrrev_i32_e32 v20, 2, v18
	v_mul_lo_u32 v18, v19, s67
	v_lshlrev_b32_e32 v19, 4, v19
	v_add3_u32 v17, s65, v18, v17
	v_add_u32_e32 v18, s4, v20
	v_mul_lo_u32 v20, v20, s67
	v_and_b32_e32 v178, 48, v19
	v_add3_u32 v30, s65, v20, v178
	v_pk_mul_f32 v[22:23], v[130:131], s[30:31] op_sel_hi:[1,0]
	v_pk_mul_f32 v[20:21], v[128:129], s[30:31] op_sel_hi:[1,0]
	v_pk_mul_f32 v[24:25], v[142:143], s[30:31] op_sel_hi:[1,0]
	v_pk_mul_f32 v[26:27], v[140:141], s[30:31] op_sel_hi:[1,0]
	v_cvt_pk_bf16_f32 v20, v20, v21
	v_cvt_pk_bf16_f32 v21, v22, v23
	v_cvt_pk_bf16_f32 v22, v26, v27
	v_cvt_pk_bf16_f32 v23, v24, v25
	ds_write_b128 v17, v[20:23]
	v_pk_mul_f32 v[22:23], v[162:163], s[30:31] op_sel_hi:[1,0]
	v_pk_mul_f32 v[20:21], v[160:161], s[30:31] op_sel_hi:[1,0]
	v_pk_mul_f32 v[24:25], v[166:167], s[30:31] op_sel_hi:[1,0]
	v_pk_mul_f32 v[26:27], v[164:165], s[30:31] op_sel_hi:[1,0]
	s_lshl_b32 s4, s35, 8
	v_cvt_pk_bf16_f32 v20, v20, v21
	v_cvt_pk_bf16_f32 v21, v22, v23
	v_cvt_pk_bf16_f32 v22, v26, v27
	v_cvt_pk_bf16_f32 v23, v24, v25
	v_ashrrev_i32_e32 v19, 31, v18
	s_ashr_i32 s5, s4, 31
	ds_write_b128 v17, v[20:23] offset:64
	v_lshlrev_b64 v[20:21], 12, v[18:19]
	v_lshl_add_u64 v[20:21], s[18:19], 0, v[20:21]
	s_lshl_b64 s[4:5], s[4:5], 1
	v_lshl_add_u64 v[28:29], v[20:21], 0, s[4:5]
	ds_read_b128 v[20:23], v30
	ds_read_b128 v[24:27], v30 offset:64
	s_mov_b32 s35, s8
	v_lshl_add_u64 v[28:29], v[28:29], 0, s[34:35]
	v_lshl_add_u64 v[28:29], v[28:29], 0, v[178:179]
	s_waitcnt lgkmcnt(0)
	global_store_dwordx4 v[28:29], v[20:23], off
	global_store_dwordx4 v[28:29], v[24:27], off offset:256
	s_nop 0
	v_pk_mul_f32 v[22:23], v[122:123], s[30:31] op_sel_hi:[1,0]
	v_pk_mul_f32 v[20:21], v[120:121], s[30:31] op_sel_hi:[1,0]
	v_pk_mul_f32 v[24:25], v[126:127], s[30:31] op_sel_hi:[1,0]
	v_pk_mul_f32 v[26:27], v[124:125], s[30:31] op_sel_hi:[1,0]
	v_cvt_pk_bf16_f32 v20, v20, v21
	v_cvt_pk_bf16_f32 v21, v22, v23
	v_cvt_pk_bf16_f32 v22, v26, v27
	v_cvt_pk_bf16_f32 v23, v24, v25
	ds_write_b128 v17, v[20:23]
	v_pk_mul_f32 v[22:23], v[146:147], s[30:31] op_sel_hi:[1,0]
	v_pk_mul_f32 v[20:21], v[144:145], s[30:31] op_sel_hi:[1,0]
	v_pk_mul_f32 v[24:25], v[150:151], s[30:31] op_sel_hi:[1,0]
	v_pk_mul_f32 v[26:27], v[148:149], s[30:31] op_sel_hi:[1,0]
	v_cvt_pk_bf16_f32 v20, v20, v21
	v_cvt_pk_bf16_f32 v21, v22, v23
	v_cvt_pk_bf16_f32 v22, v26, v27
	v_cvt_pk_bf16_f32 v23, v24, v25
	ds_write_b128 v17, v[20:23] offset:64
	v_add_u32_e32 v20, 16, v18
	v_ashrrev_i32_e32 v21, 31, v20
	v_lshlrev_b64 v[20:21], 12, v[20:21]
	v_lshl_add_u64 v[28:29], s[18:19], 0, v[20:21]
	ds_read_b128 v[20:23], v30
	ds_read_b128 v[24:27], v30 offset:64
	v_lshl_add_u64 v[28:29], v[28:29], 0, s[4:5]
	v_lshl_add_u64 v[28:29], v[28:29], 0, s[34:35]
	v_lshl_add_u64 v[28:29], v[28:29], 0, v[178:179]
	s_waitcnt lgkmcnt(0)
	global_store_dwordx4 v[28:29], v[20:23], off
	global_store_dwordx4 v[28:29], v[24:27], off offset:256
	s_nop 0
	v_pk_mul_f32 v[22:23], v[98:99], s[30:31] op_sel_hi:[1,0]
	v_pk_mul_f32 v[20:21], v[96:97], s[30:31] op_sel_hi:[1,0]
	v_pk_mul_f32 v[24:25], v[102:103], s[30:31] op_sel_hi:[1,0]
	v_pk_mul_f32 v[26:27], v[100:101], s[30:31] op_sel_hi:[1,0]
	v_cvt_pk_bf16_f32 v20, v20, v21
	v_cvt_pk_bf16_f32 v21, v22, v23
	v_cvt_pk_bf16_f32 v22, v26, v27
	v_cvt_pk_bf16_f32 v23, v24, v25
	ds_write_b128 v17, v[20:23]
	v_pk_mul_f32 v[22:23], v[134:135], s[30:31] op_sel_hi:[1,0]
	v_pk_mul_f32 v[20:21], v[132:133], s[30:31] op_sel_hi:[1,0]
	v_pk_mul_f32 v[24:25], v[138:139], s[30:31] op_sel_hi:[1,0]
	v_pk_mul_f32 v[26:27], v[136:137], s[30:31] op_sel_hi:[1,0]
	v_cvt_pk_bf16_f32 v20, v20, v21
	v_cvt_pk_bf16_f32 v21, v22, v23
	v_cvt_pk_bf16_f32 v22, v26, v27
	v_cvt_pk_bf16_f32 v23, v24, v25
	ds_write_b128 v17, v[20:23] offset:64
	v_add_u32_e32 v20, 32, v18
	v_ashrrev_i32_e32 v21, 31, v20
	v_lshlrev_b64 v[20:21], 12, v[20:21]
	v_lshl_add_u64 v[28:29], s[18:19], 0, v[20:21]
	ds_read_b128 v[20:23], v30
	ds_read_b128 v[24:27], v30 offset:64
	v_lshl_add_u64 v[28:29], v[28:29], 0, s[4:5]
	v_lshl_add_u64 v[28:29], v[28:29], 0, s[34:35]
	v_lshl_add_u64 v[28:29], v[28:29], 0, v[178:179]
	s_waitcnt lgkmcnt(0)
	global_store_dwordx4 v[28:29], v[20:23], off
	global_store_dwordx4 v[28:29], v[24:27], off offset:256
	s_nop 0
	v_pk_mul_f32 v[22:23], v[82:83], s[30:31] op_sel_hi:[1,0]
	v_pk_mul_f32 v[20:21], v[80:81], s[30:31] op_sel_hi:[1,0]
	v_pk_mul_f32 v[24:25], v[86:87], s[30:31] op_sel_hi:[1,0]
	v_pk_mul_f32 v[26:27], v[84:85], s[30:31] op_sel_hi:[1,0]
	v_cvt_pk_bf16_f32 v20, v20, v21
	v_cvt_pk_bf16_f32 v21, v22, v23
	v_cvt_pk_bf16_f32 v22, v26, v27
	v_cvt_pk_bf16_f32 v23, v24, v25
	ds_write_b128 v17, v[20:23]
	v_pk_mul_f32 v[22:23], v[106:107], s[30:31] op_sel_hi:[1,0]
	v_pk_mul_f32 v[20:21], v[104:105], s[30:31] op_sel_hi:[1,0]
	v_pk_mul_f32 v[24:25], v[110:111], s[30:31] op_sel_hi:[1,0]
	v_pk_mul_f32 v[26:27], v[108:109], s[30:31] op_sel_hi:[1,0]
	v_cvt_pk_bf16_f32 v20, v20, v21
	v_cvt_pk_bf16_f32 v21, v22, v23
	v_cvt_pk_bf16_f32 v22, v26, v27
	v_cvt_pk_bf16_f32 v23, v24, v25
	ds_write_b128 v17, v[20:23] offset:64
	v_add_u32_e32 v20, 48, v18
	v_ashrrev_i32_e32 v21, 31, v20
	v_lshlrev_b64 v[20:21], 12, v[20:21]
	v_lshl_add_u64 v[28:29], s[18:19], 0, v[20:21]
	ds_read_b128 v[20:23], v30
	ds_read_b128 v[24:27], v30 offset:64
	v_lshl_add_u64 v[28:29], v[28:29], 0, s[4:5]
	v_lshl_add_u64 v[28:29], v[28:29], 0, s[34:35]
	v_lshl_add_u64 v[28:29], v[28:29], 0, v[178:179]
	s_waitcnt lgkmcnt(0)
	global_store_dwordx4 v[28:29], v[20:23], off
	global_store_dwordx4 v[28:29], v[24:27], off offset:256
	s_nop 0
	v_pk_mul_f32 v[22:23], v[114:115], s[30:31] op_sel_hi:[1,0]
	v_pk_mul_f32 v[20:21], v[112:113], s[30:31] op_sel_hi:[1,0]
	v_pk_mul_f32 v[26:27], v[118:119], s[30:31] op_sel_hi:[1,0]
	v_pk_mul_f32 v[28:29], v[116:117], s[30:31] op_sel_hi:[1,0]
	v_cvt_pk_bf16_f32 v20, v20, v21
	v_cvt_pk_bf16_f32 v21, v22, v23
	v_cvt_pk_bf16_f32 v22, v28, v29
	v_cvt_pk_bf16_f32 v23, v26, v27
	v_add_u32_e32 v24, 0x80, v18
	ds_write_b128 v17, v[20:23]
	v_pk_mul_f32 v[22:23], v[154:155], s[30:31] op_sel_hi:[1,0]
	v_pk_mul_f32 v[20:21], v[152:153], s[30:31] op_sel_hi:[1,0]
	v_pk_mul_f32 v[26:27], v[158:159], s[30:31] op_sel_hi:[1,0]
	v_pk_mul_f32 v[28:29], v[156:157], s[30:31] op_sel_hi:[1,0]
	v_cvt_pk_bf16_f32 v20, v20, v21
	v_cvt_pk_bf16_f32 v21, v22, v23
	v_cvt_pk_bf16_f32 v22, v28, v29
	v_cvt_pk_bf16_f32 v23, v26, v27
	v_ashrrev_i32_e32 v25, 31, v24
	ds_write_b128 v17, v[20:23] offset:64
	v_lshlrev_b64 v[20:21], 12, v[24:25]
	v_lshl_add_u64 v[28:29], s[18:19], 0, v[20:21]
	ds_read_b128 v[20:23], v30
	ds_read_b128 v[24:27], v30 offset:64
	v_lshl_add_u64 v[28:29], v[28:29], 0, s[4:5]
	v_lshl_add_u64 v[28:29], v[28:29], 0, s[34:35]
	v_lshl_add_u64 v[28:29], v[28:29], 0, v[178:179]
	s_waitcnt lgkmcnt(0)
	global_store_dwordx4 v[28:29], v[20:23], off
	global_store_dwordx4 v[28:29], v[24:27], off offset:256
	s_nop 0
	v_pk_mul_f32 v[22:23], v[90:91], s[30:31] op_sel_hi:[1,0]
	v_pk_mul_f32 v[20:21], v[88:89], s[30:31] op_sel_hi:[1,0]
	v_pk_mul_f32 v[24:25], v[94:95], s[30:31] op_sel_hi:[1,0]
	v_pk_mul_f32 v[26:27], v[92:93], s[30:31] op_sel_hi:[1,0]
	v_cvt_pk_bf16_f32 v20, v20, v21
	v_cvt_pk_bf16_f32 v21, v22, v23
	v_cvt_pk_bf16_f32 v22, v26, v27
	v_cvt_pk_bf16_f32 v23, v24, v25
	ds_write_b128 v17, v[20:23]
	v_pk_mul_f32 v[22:23], v[58:59], s[30:31] op_sel_hi:[1,0]
	v_pk_mul_f32 v[20:21], v[56:57], s[30:31] op_sel_hi:[1,0]
	v_pk_mul_f32 v[24:25], v[62:63], s[30:31] op_sel_hi:[1,0]
	v_pk_mul_f32 v[26:27], v[60:61], s[30:31] op_sel_hi:[1,0]
	v_cvt_pk_bf16_f32 v20, v20, v21
	v_cvt_pk_bf16_f32 v21, v22, v23
	v_cvt_pk_bf16_f32 v22, v26, v27
	v_cvt_pk_bf16_f32 v23, v24, v25
	ds_write_b128 v17, v[20:23] offset:64
	v_add_u32_e32 v20, 0x90, v18
	v_ashrrev_i32_e32 v21, 31, v20
	v_lshlrev_b64 v[20:21], 12, v[20:21]
	v_lshl_add_u64 v[28:29], s[18:19], 0, v[20:21]
	ds_read_b128 v[20:23], v30
	ds_read_b128 v[24:27], v30 offset:64
	v_lshl_add_u64 v[28:29], v[28:29], 0, s[4:5]
	v_lshl_add_u64 v[28:29], v[28:29], 0, s[34:35]
	v_pk_mul_f32 v[10:11], v[10:11], s[30:31] op_sel_hi:[1,0]
	v_pk_mul_f32 v[8:9], v[8:9], s[30:31] op_sel_hi:[1,0]
	v_pk_mul_f32 v[14:15], v[14:15], s[30:31] op_sel_hi:[1,0]
	v_pk_mul_f32 v[12:13], v[12:13], s[30:31] op_sel_hi:[1,0]
	v_lshl_add_u64 v[28:29], v[28:29], 0, v[178:179]
	v_cvt_pk_bf16_f32 v8, v8, v9
	v_cvt_pk_bf16_f32 v9, v10, v11
	v_cvt_pk_bf16_f32 v10, v12, v13
	v_cvt_pk_bf16_f32 v11, v14, v15
	s_waitcnt lgkmcnt(0)
	global_store_dwordx4 v[28:29], v[20:23], off
	global_store_dwordx4 v[28:29], v[24:27], off offset:256
	ds_write_b128 v17, v[8:11] offset:64
	v_pk_mul_f32 v[22:23], v[74:75], s[30:31] op_sel_hi:[1,0]
	v_pk_mul_f32 v[20:21], v[72:73], s[30:31] op_sel_hi:[1,0]
	v_pk_mul_f32 v[24:25], v[78:79], s[30:31] op_sel_hi:[1,0]
	v_pk_mul_f32 v[26:27], v[76:77], s[30:31] op_sel_hi:[1,0]
	v_add_u32_e32 v8, 0xa0, v18
	v_cvt_pk_bf16_f32 v20, v20, v21
	v_cvt_pk_bf16_f32 v21, v22, v23
	v_cvt_pk_bf16_f32 v22, v26, v27
	v_cvt_pk_bf16_f32 v23, v24, v25
	v_ashrrev_i32_e32 v9, 31, v8
	ds_write_b128 v17, v[20:23]
	v_lshlrev_b64 v[8:9], 12, v[8:9]
	v_lshl_add_u64 v[20:21], s[18:19], 0, v[8:9]
	ds_read_b128 v[8:11], v30
	ds_read_b128 v[12:15], v30 offset:64
	v_lshl_add_u64 v[20:21], v[20:21], 0, s[4:5]
	v_lshl_add_u64 v[20:21], v[20:21], 0, s[34:35]
	v_lshl_add_u64 v[20:21], v[20:21], 0, v[178:179]
	s_waitcnt lgkmcnt(0)
	global_store_dwordx4 v[20:21], v[8:11], off
	global_store_dwordx4 v[20:21], v[12:15], off offset:256
	s_nop 0
	v_pk_mul_f32 v[10:11], v[70:71], s[30:31] op_sel_hi:[1,0]
	v_pk_mul_f32 v[8:9], v[68:69], s[30:31] op_sel_hi:[1,0]
	v_pk_mul_f32 v[12:13], v[66:67], s[30:31] op_sel_hi:[1,0]
	v_pk_mul_f32 v[14:15], v[64:65], s[30:31] op_sel_hi:[1,0]
	v_cvt_pk_bf16_f32 v8, v8, v9
	v_cvt_pk_bf16_f32 v9, v10, v11
	v_cvt_pk_bf16_f32 v10, v14, v15
	v_cvt_pk_bf16_f32 v11, v12, v13
	ds_write_b128 v17, v[8:11]
	v_pk_mul_f32 v[6:7], v[6:7], s[30:31] op_sel_hi:[1,0]
	v_pk_mul_f32 v[4:5], v[4:5], s[30:31] op_sel_hi:[1,0]
	v_pk_mul_f32 v[8:9], v[2:3], s[30:31] op_sel_hi:[1,0]
	v_pk_mul_f32 v[2:3], v[0:1], s[30:31] op_sel_hi:[1,0]
	v_cvt_pk_bf16_f32 v0, v4, v5
	v_cvt_pk_bf16_f32 v1, v6, v7
	v_cvt_pk_bf16_f32 v2, v2, v3
	v_cvt_pk_bf16_f32 v3, v8, v9
	ds_write_b128 v17, v[0:3] offset:64
	v_add_u32_e32 v0, 0xb0, v18
	v_ashrrev_i32_e32 v1, 31, v0
	v_lshlrev_b64 v[0:1], 12, v[0:1]
	v_lshl_add_u64 v[8:9], s[18:19], 0, v[0:1]
	ds_read_b128 v[0:3], v30
	ds_read_b128 v[4:7], v30 offset:64
	v_lshl_add_u64 v[8:9], v[8:9], 0, s[4:5]
	v_lshl_add_u64 v[8:9], v[8:9], 0, s[34:35]
	v_lshl_add_u64 v[8:9], v[8:9], 0, v[178:179]
	s_mov_b64 s[4:5], -1
	s_andn2_b64 vcc, exec, s[2:3]
	s_mov_b32 s35, s36
	s_mov_b32 s44, s38
	s_mov_b64 s[46:47], s[42:43]
	s_mov_b64 s[48:49], s[40:41]
	s_waitcnt lgkmcnt(0)
	global_store_dwordx4 v[8:9], v[0:3], off
	global_store_dwordx4 v[8:9], v[4:7], off offset:256
	s_cbranch_vccz .LBB0_2410

.LBB0_2750:
	v_mov_b32_e32 v17, v186
	v_mov_b32_e32 v19, v187
	s_nop 15
	s_nop 15
	v_pk_mul_f32 v[24:25], v[140:141], s[30:31] op_sel_hi:[1,0]
	v_lshl_add_u32 v18, v17, 4, v19
	v_ashrrev_i32_e32 v18, 2, v18
	v_and_b32_e32 v20, 3, v19
	v_mul_lo_u32 v21, v19, s71
	v_lshlrev_b32_e32 v17, 3, v17
	v_add3_u32 v17, s68, v21, v17
	v_mul_lo_u32 v21, v18, s71
	v_lshlrev_b32_e32 v20, 4, v20
	v_add3_u32 v22, s68, v21, v20
	v_lshlrev_b32_e32 v20, 6, v19
	v_and_b32_e32 v180, 0x80, v20
	v_pk_mul_f32 v[20:21], v[136:137], s[30:31] op_sel_hi:[1,0]
	v_mov_b32_e32 v26, v181
	v_mov_b32_e32 v27, v181
	v_cvt_pk_fp8_f32 v26, v20, v21
	v_cvt_pk_fp8_f32 v27, v24, v25
	v_pk_mul_f32 v[20:21], v[138:139], s[30:31] op_sel_hi:[1,0]
	v_pk_mul_f32 v[24:25], v[142:143], s[30:31] op_sel_hi:[1,0]
	v_cvt_pk_fp8_f32 v26, v20, v21 op_sel:[0,0,1]
	v_cvt_pk_fp8_f32 v27, v24, v25 op_sel:[0,0,1]
	v_pk_mul_f32 v[20:21], v[160:161], s[30:31] op_sel_hi:[1,0]
	v_pk_mul_f32 v[24:25], v[164:165], s[30:31] op_sel_hi:[1,0]
	v_mov_b32_e32 v28, v181
	v_mov_b32_e32 v29, v181
	v_cvt_pk_fp8_f32 v28, v20, v21
	v_cvt_pk_fp8_f32 v29, v24, v25
	v_pk_mul_f32 v[30:31], v[120:121], s[30:31] op_sel_hi:[1,0]
	v_pk_mul_f32 v[32:33], v[124:125], s[30:31] op_sel_hi:[1,0]
	v_mov_b32_e32 v34, v181
	v_mov_b32_e32 v35, v181
	v_cvt_pk_fp8_f32 v34, v30, v31
	v_cvt_pk_fp8_f32 v35, v32, v33
	s_lshl_b32 s6, s42, 8
	v_pk_mul_f32 v[20:21], v[162:163], s[30:31] op_sel_hi:[1,0]
	v_pk_mul_f32 v[24:25], v[166:167], s[30:31] op_sel_hi:[1,0]
	s_add_i32 s6, s6, s65
	v_cvt_pk_fp8_f32 v28, v20, v21 op_sel:[0,0,1]
	v_cvt_pk_fp8_f32 v29, v24, v25 op_sel:[0,0,1]
	v_pk_mul_f32 v[30:31], v[122:123], s[30:31] op_sel_hi:[1,0]
	v_pk_mul_f32 v[32:33], v[126:127], s[30:31] op_sel_hi:[1,0]
	v_add_u32_e32 v18, s6, v18
	v_lshlrev_b32_e32 v19, 4, v19
	v_cvt_pk_fp8_f32 v34, v30, v31 op_sel:[0,0,1]
	v_cvt_pk_fp8_f32 v35, v32, v33 op_sel:[0,0,1]
	v_pk_mul_f32 v[30:31], v[144:145], s[30:31] op_sel_hi:[1,0]
	v_pk_mul_f32 v[32:33], v[152:153], s[30:31] op_sel_hi:[1,0]
	v_mov_b32_e32 v36, v181
	v_mov_b32_e32 v37, v181
	v_and_b32_e32 v20, 16, v19
	v_ashrrev_i32_e32 v19, 31, v18
	v_cvt_pk_fp8_f32 v36, v30, v31
	v_cvt_pk_fp8_f32 v37, v32, v33
	s_lshl_b32 s6, s44, 8
	ds_write_b64 v17, v[26:27]
	ds_write_b64 v17, v[28:29] offset:32
	v_lshlrev_b64 v[28:29], 11, v[18:19]
	s_ashr_i32 s7, s6, 31
	ds_read_b128 v[24:27], v22
	v_lshl_add_u64 v[28:29], s[20:21], 0, v[28:29]
	v_lshl_add_u64 v[28:29], v[28:29], 0, s[6:7]
	v_pk_mul_f32 v[30:31], v[146:147], s[30:31] op_sel_hi:[1,0]
	v_pk_mul_f32 v[32:33], v[154:155], s[30:31] op_sel_hi:[1,0]
	v_lshl_add_u64 v[28:29], v[28:29], 0, v[180:181]
	v_cvt_pk_fp8_f32 v36, v30, v31 op_sel:[0,0,1]
	v_cvt_pk_fp8_f32 v37, v32, v33 op_sel:[0,0,1]
	v_mov_b32_e32 v21, v181
	v_lshl_add_u64 v[28:29], v[28:29], 0, s[18:19]
	v_lshl_add_u64 v[28:29], v[28:29], 0, v[20:21]
	s_waitcnt lgkmcnt(0)
	global_store_dwordx4 v[28:29], v[24:27], off
	ds_write_b64 v17, v[34:35]
	ds_write_b64 v17, v[36:37] offset:32
	v_pk_mul_f32 v[30:31], v[96:97], s[30:31] op_sel_hi:[1,0]
	v_pk_mul_f32 v[32:33], v[100:101], s[30:31] op_sel_hi:[1,0]
	v_mov_b32_e32 v34, v181
	v_mov_b32_e32 v35, v181
	v_cvt_pk_fp8_f32 v34, v30, v31
	v_cvt_pk_fp8_f32 v35, v32, v33
	v_pk_mul_f32 v[30:31], v[98:99], s[30:31] op_sel_hi:[1,0]
	v_pk_mul_f32 v[32:33], v[102:103], s[30:31] op_sel_hi:[1,0]
	v_add_u32_e32 v28, 16, v18
	v_cvt_pk_fp8_f32 v34, v30, v31 op_sel:[0,0,1]
	v_cvt_pk_fp8_f32 v35, v32, v33 op_sel:[0,0,1]
	v_pk_mul_f32 v[30:31], v[128:129], s[30:31] op_sel_hi:[1,0]
	v_pk_mul_f32 v[32:33], v[132:133], s[30:31] op_sel_hi:[1,0]
	v_mov_b32_e32 v36, v181
	v_mov_b32_e32 v37, v181
	v_ashrrev_i32_e32 v29, 31, v28
	v_cvt_pk_fp8_f32 v36, v30, v31
	v_cvt_pk_fp8_f32 v37, v32, v33
	v_lshlrev_b64 v[28:29], 11, v[28:29]
	ds_read_b128 v[24:27], v22
	v_lshl_add_u64 v[28:29], s[20:21], 0, v[28:29]
	v_lshl_add_u64 v[28:29], v[28:29], 0, s[6:7]
	v_pk_mul_f32 v[30:31], v[130:131], s[30:31] op_sel_hi:[1,0]
	v_pk_mul_f32 v[32:33], v[134:135], s[30:31] op_sel_hi:[1,0]
	v_lshl_add_u64 v[28:29], v[28:29], 0, v[180:181]
	v_cvt_pk_fp8_f32 v36, v30, v31 op_sel:[0,0,1]
	v_cvt_pk_fp8_f32 v37, v32, v33 op_sel:[0,0,1]
	v_lshl_add_u64 v[28:29], v[28:29], 0, s[18:19]
	v_lshl_add_u64 v[28:29], v[28:29], 0, v[20:21]
	s_waitcnt lgkmcnt(0)
	global_store_dwordx4 v[28:29], v[24:27], off
	ds_write_b64 v17, v[34:35]
	ds_write_b64 v17, v[36:37] offset:32
	v_pk_mul_f32 v[30:31], v[80:81], s[30:31] op_sel_hi:[1,0]
	v_pk_mul_f32 v[32:33], v[84:85], s[30:31] op_sel_hi:[1,0]
	v_mov_b32_e32 v34, v181
	v_mov_b32_e32 v35, v181
	v_cvt_pk_fp8_f32 v34, v30, v31
	v_cvt_pk_fp8_f32 v35, v32, v33
	v_pk_mul_f32 v[30:31], v[82:83], s[30:31] op_sel_hi:[1,0]
	v_pk_mul_f32 v[32:33], v[86:87], s[30:31] op_sel_hi:[1,0]
	v_add_u32_e32 v28, 32, v18
	v_cvt_pk_fp8_f32 v34, v30, v31 op_sel:[0,0,1]
	v_cvt_pk_fp8_f32 v35, v32, v33 op_sel:[0,0,1]
	v_pk_mul_f32 v[30:31], v[104:105], s[30:31] op_sel_hi:[1,0]
	v_pk_mul_f32 v[32:33], v[112:113], s[30:31] op_sel_hi:[1,0]
	v_mov_b32_e32 v36, v181
	v_mov_b32_e32 v37, v181
	v_ashrrev_i32_e32 v29, 31, v28
	v_cvt_pk_fp8_f32 v36, v30, v31
	v_cvt_pk_fp8_f32 v37, v32, v33
	v_lshlrev_b64 v[28:29], 11, v[28:29]
	ds_read_b128 v[24:27], v22
	v_lshl_add_u64 v[28:29], s[20:21], 0, v[28:29]
	v_lshl_add_u64 v[28:29], v[28:29], 0, s[6:7]
	v_pk_mul_f32 v[30:31], v[106:107], s[30:31] op_sel_hi:[1,0]
	v_pk_mul_f32 v[32:33], v[114:115], s[30:31] op_sel_hi:[1,0]
	v_lshl_add_u64 v[28:29], v[28:29], 0, v[180:181]
	v_cvt_pk_fp8_f32 v36, v30, v31 op_sel:[0,0,1]
	v_cvt_pk_fp8_f32 v37, v32, v33 op_sel:[0,0,1]
	v_lshl_add_u64 v[28:29], v[28:29], 0, s[18:19]
	v_lshl_add_u64 v[28:29], v[28:29], 0, v[20:21]
	s_waitcnt lgkmcnt(0)
	global_store_dwordx4 v[28:29], v[24:27], off
	ds_write_b64 v17, v[34:35]
	ds_write_b64 v17, v[36:37] offset:32
	v_pk_mul_f32 v[30:31], v[108:109], s[30:31] op_sel_hi:[1,0]
	v_pk_mul_f32 v[32:33], v[116:117], s[30:31] op_sel_hi:[1,0]
	v_mov_b32_e32 v34, v181
	v_mov_b32_e32 v35, v181
	v_cvt_pk_fp8_f32 v34, v30, v31
	v_cvt_pk_fp8_f32 v35, v32, v33
	v_pk_mul_f32 v[30:31], v[110:111], s[30:31] op_sel_hi:[1,0]
	v_pk_mul_f32 v[32:33], v[118:119], s[30:31] op_sel_hi:[1,0]
	v_add_u32_e32 v28, 48, v18
	v_cvt_pk_fp8_f32 v34, v30, v31 op_sel:[0,0,1]
	v_cvt_pk_fp8_f32 v35, v32, v33 op_sel:[0,0,1]
	v_pk_mul_f32 v[30:31], v[148:149], s[30:31] op_sel_hi:[1,0]
	v_pk_mul_f32 v[32:33], v[156:157], s[30:31] op_sel_hi:[1,0]
	v_mov_b32_e32 v36, v181
	v_mov_b32_e32 v37, v181
	v_ashrrev_i32_e32 v29, 31, v28
	v_cvt_pk_fp8_f32 v36, v30, v31
	v_cvt_pk_fp8_f32 v37, v32, v33
	v_lshlrev_b64 v[28:29], 11, v[28:29]
	ds_read_b128 v[24:27], v22
	v_lshl_add_u64 v[28:29], s[20:21], 0, v[28:29]
	v_lshl_add_u64 v[28:29], v[28:29], 0, s[6:7]
	v_pk_mul_f32 v[30:31], v[150:151], s[30:31] op_sel_hi:[1,0]
	v_pk_mul_f32 v[32:33], v[158:159], s[30:31] op_sel_hi:[1,0]
	v_lshl_add_u64 v[28:29], v[28:29], 0, v[180:181]
	v_cvt_pk_fp8_f32 v36, v30, v31 op_sel:[0,0,1]
	v_cvt_pk_fp8_f32 v37, v32, v33 op_sel:[0,0,1]
	v_lshl_add_u64 v[28:29], v[28:29], 0, s[18:19]
	v_lshl_add_u64 v[28:29], v[28:29], 0, v[20:21]
	s_waitcnt lgkmcnt(0)
	global_store_dwordx4 v[28:29], v[24:27], off
	ds_write_b64 v17, v[34:35]
	ds_write_b64 v17, v[36:37] offset:32
	v_pk_mul_f32 v[30:31], v[88:89], s[30:31] op_sel_hi:[1,0]
	v_pk_mul_f32 v[32:33], v[92:93], s[30:31] op_sel_hi:[1,0]
	v_mov_b32_e32 v34, v181
	v_mov_b32_e32 v35, v181
	v_cvt_pk_fp8_f32 v34, v30, v31
	v_cvt_pk_fp8_f32 v35, v32, v33
	v_pk_mul_f32 v[30:31], v[90:91], s[30:31] op_sel_hi:[1,0]
	v_pk_mul_f32 v[32:33], v[94:95], s[30:31] op_sel_hi:[1,0]
	v_add_u32_e32 v28, 0x80, v18
	v_cvt_pk_fp8_f32 v34, v30, v31 op_sel:[0,0,1]
	v_cvt_pk_fp8_f32 v35, v32, v33 op_sel:[0,0,1]
	v_pk_mul_f32 v[30:31], v[56:57], s[30:31] op_sel_hi:[1,0]
	v_pk_mul_f32 v[32:33], v[60:61], s[30:31] op_sel_hi:[1,0]
	v_mov_b32_e32 v36, v181
	v_mov_b32_e32 v37, v181
	v_ashrrev_i32_e32 v29, 31, v28
	v_cvt_pk_fp8_f32 v36, v30, v31
	v_cvt_pk_fp8_f32 v37, v32, v33
	v_lshlrev_b64 v[28:29], 11, v[28:29]
	ds_read_b128 v[24:27], v22
	v_lshl_add_u64 v[28:29], s[20:21], 0, v[28:29]
	v_lshl_add_u64 v[28:29], v[28:29], 0, s[6:7]
	v_pk_mul_f32 v[30:31], v[58:59], s[30:31] op_sel_hi:[1,0]
	v_pk_mul_f32 v[32:33], v[62:63], s[30:31] op_sel_hi:[1,0]
	v_lshl_add_u64 v[28:29], v[28:29], 0, v[180:181]
	v_cvt_pk_fp8_f32 v36, v30, v31 op_sel:[0,0,1]
	v_cvt_pk_fp8_f32 v37, v32, v33 op_sel:[0,0,1]
	v_lshl_add_u64 v[28:29], v[28:29], 0, s[18:19]
	v_lshl_add_u64 v[28:29], v[28:29], 0, v[20:21]
	s_waitcnt lgkmcnt(0)
	global_store_dwordx4 v[28:29], v[24:27], off
	ds_write_b64 v17, v[34:35]
	ds_write_b64 v17, v[36:37] offset:32
	v_pk_mul_f32 v[30:31], v[72:73], s[30:31] op_sel_hi:[1,0]
	v_mov_b32_e32 v34, v181
	v_cvt_pk_fp8_f32 v34, v30, v31
	v_add_u32_e32 v28, 0x90, v18
	v_ashrrev_i32_e32 v29, 31, v28
	v_pk_mul_f32 v[30:31], v[74:75], s[30:31] op_sel_hi:[1,0]
	v_lshlrev_b64 v[28:29], 11, v[28:29]
	v_cvt_pk_fp8_f32 v34, v30, v31 op_sel:[0,0,1]
	v_pk_mul_f32 v[8:9], v[8:9], s[30:31] op_sel_hi:[1,0]
	v_mov_b32_e32 v30, v181
	ds_read_b128 v[24:27], v22
	v_lshl_add_u64 v[28:29], s[20:21], 0, v[28:29]
	v_cvt_pk_fp8_f32 v30, v8, v9
	v_lshl_add_u64 v[28:29], v[28:29], 0, s[6:7]
	v_lshl_add_u64 v[28:29], v[28:29], 0, v[180:181]
	v_lshl_add_u64 v[28:29], v[28:29], 0, s[18:19]
	v_pk_mul_f32 v[32:33], v[76:77], s[30:31] op_sel_hi:[1,0]
	v_mov_b32_e32 v35, v181
	v_pk_mul_f32 v[8:9], v[10:11], s[30:31] op_sel_hi:[1,0]
	v_cvt_pk_fp8_f32 v35, v32, v33
	v_pk_mul_f32 v[12:13], v[12:13], s[30:31] op_sel_hi:[1,0]
	v_mov_b32_e32 v31, v181
	v_cvt_pk_fp8_f32 v30, v8, v9 op_sel:[0,0,1]
	v_lshl_add_u64 v[8:9], v[28:29], 0, v[20:21]
	v_cvt_pk_fp8_f32 v31, v12, v13
	v_pk_mul_f32 v[10:11], v[14:15], s[30:31] op_sel_hi:[1,0]
	s_waitcnt lgkmcnt(0)
	global_store_dwordx4 v[8:9], v[24:27], off
	v_pk_mul_f32 v[14:15], v[68:69], s[30:31] op_sel_hi:[1,0]
	v_pk_mul_f32 v[32:33], v[78:79], s[30:31] op_sel_hi:[1,0]
	v_mov_b32_e32 v26, v181
	v_cvt_pk_fp8_f32 v26, v14, v15
	v_cvt_pk_fp8_f32 v35, v32, v33 op_sel:[0,0,1]
	v_cvt_pk_fp8_f32 v31, v10, v11 op_sel:[0,0,1]
	v_pk_mul_f32 v[24:25], v[64:65], s[30:31] op_sel_hi:[1,0]
	v_mov_b32_e32 v27, v181
	v_pk_mul_f32 v[14:15], v[70:71], s[30:31] op_sel_hi:[1,0]
	v_add_u32_e32 v12, 0xa0, v18
	v_cvt_pk_fp8_f32 v27, v24, v25
	v_cvt_pk_fp8_f32 v26, v14, v15 op_sel:[0,0,1]
	v_pk_mul_f32 v[4:5], v[4:5], s[30:31] op_sel_hi:[1,0]
	v_pk_mul_f32 v[0:1], v[0:1], s[30:31] op_sel_hi:[1,0]
	v_mov_b32_e32 v14, v181
	v_mov_b32_e32 v15, v181
	v_ashrrev_i32_e32 v13, 31, v12
	v_cvt_pk_fp8_f32 v14, v4, v5
	v_cvt_pk_fp8_f32 v15, v0, v1
	ds_write_b64 v17, v[34:35]
	ds_write_b64 v17, v[30:31] offset:32
	v_lshlrev_b64 v[12:13], 11, v[12:13]
	ds_read_b128 v[8:11], v22
	v_lshl_add_u64 v[12:13], s[20:21], 0, v[12:13]
	v_pk_mul_f32 v[24:25], v[66:67], s[30:31] op_sel_hi:[1,0]
	v_lshl_add_u64 v[12:13], v[12:13], 0, s[6:7]
	v_cvt_pk_fp8_f32 v27, v24, v25 op_sel:[0,0,1]
	v_pk_mul_f32 v[0:1], v[6:7], s[30:31] op_sel_hi:[1,0]
	v_pk_mul_f32 v[2:3], v[2:3], s[30:31] op_sel_hi:[1,0]
	v_lshl_add_u64 v[12:13], v[12:13], 0, v[180:181]
	v_cvt_pk_fp8_f32 v14, v0, v1 op_sel:[0,0,1]
	v_cvt_pk_fp8_f32 v15, v2, v3 op_sel:[0,0,1]
	v_lshl_add_u64 v[12:13], v[12:13], 0, s[18:19]
	v_add_u32_e32 v4, 0xb0, v18
	v_lshl_add_u64 v[0:1], v[12:13], 0, v[20:21]
	v_ashrrev_i32_e32 v5, 31, v4
	s_waitcnt lgkmcnt(0)
	global_store_dwordx4 v[0:1], v[8:11], off
	ds_write_b64 v17, v[26:27]
	ds_write_b64 v17, v[14:15] offset:32
	v_lshlrev_b64 v[4:5], 11, v[4:5]
	ds_read_b128 v[0:3], v22
	v_lshl_add_u64 v[4:5], s[20:21], 0, v[4:5]
	v_lshl_add_u64 v[4:5], v[4:5], 0, s[6:7]
	v_lshl_add_u64 v[4:5], v[4:5], 0, v[180:181]
	v_lshl_add_u64 v[4:5], v[4:5], 0, s[18:19]
	v_lshl_add_u64 v[4:5], v[4:5], 0, v[20:21]
	s_mov_b64 s[6:7], -1
	s_andn2_b64 vcc, exec, s[4:5]
	s_mov_b32 s44, s36
	s_mov_b32 s42, s34
	s_mov_b64 s[48:49], s[40:41]
	s_mov_b64 s[50:51], s[38:39]
	s_waitcnt lgkmcnt(0)
	global_store_dwordx4 v[4:5], v[0:3], off
	s_cbranch_vccz .LBB0_2765
